# attention loops: one workgroup barrier per KV tile (own-DMA wait before it), second barrier of the slot removed
# speedup vs baseline: 1.0360x; 1.0143x over previous
; #define SBAR() __builtin_amdgcn_sched_barrier(0)
; __device__ __forceinline__ void finishSM(f32x16& p0, f32x16& p1, float alpha, float& l_reg, bf16x8& pa0, bf16x8& pa1, bf16x8& pa2, bf16x8& pa3) {
;   for (int r = 0; r < 16; ++r) p1[r] = __builtin_amdgcn_exp2f(p1[r]);
;   float ps = 0; for (int r = 0; r < 16; ++r) ps += p0[r]; for (int r = 0; r < 16; ++r) ps += p1[r];
;   { auto rr = __builtin_amdgcn_permlane32_swap(__float_as_uint(ps), __float_as_uint(ps), false, false);
;     ps = __uint_as_float(rr[0]) + __uint_as_float(rr[1]); }
;   l_reg = l_reg * alpha + ps;
;     ...
;   PK4(p0, 0, pa0); PK4(p0, 8, pa1); PK4(p1, 0, pa2); PK4(p1, 8, pa3);
; template <bool HALF> __device__ __forceinline__ void qkt(f32x16& p0, f32x16& p1, const char* Ks, const bf16x8* qr, int r32, int hi, int koff) {
;   p0 = f32x16{}; p1 = f32x16{};
;   for (int d0 = 0; d0 < (HALF ? 4 : 8); ++d0) { int cb = (d0 * 16 + hi * 8) * 2 + koff;
;     bf16x8 b0 = *reinterpret_cast<const bf16x8*>(Ks + KSWZ(r32, cb));
;     bf16x8 b1 = *reinterpret_cast<const bf16x8*>(Ks + KSWZ(32 + r32, cb));
;     p0 = __builtin_amdgcn_mfma_f32_32x32x16_bf16(b0, qr[d0], p0, 0, 0, 0);
;     p1 = __builtin_amdgcn_mfma_f32_32x32x16_bf16(b1, qr[d0], p1, 0, 0, 0); }
; template <bool HALF> __device__ __forceinline__ void dense_body(const bf16_t* __restrict__ Qb, const bf16_t* __restrict__ Kh, const bf16_t* __restrict__ Vh, ...
;     ...
;     SBAR(); qkt<HALF>(pB0, pB1, Kl1, qr, r32, hi, koff);
;     finishSM(pA0, pA1, alA, l_reg, pa0, pa1, pa2, pa3); SBAR();
;     SLOAD(SO, (j + 2) * KVBLK); SBAR();
;     pv_d0(o, vb0, pa0, pa1, pa2, pa3); partialSM(pB0, pB1, m_reg, mnB, alB);
.LBB0_425:
	ds_read_b128 v[64:67], v209 offset:49152
	ds_read_b128 v[68:71], v209 offset:57344
	ds_read_b128 v[190:193], v221 offset:49152
	ds_read_b128 v[228:231], v221 offset:57344
	v_add_f32_e32 v162, 0, v163
	v_add_f32_e32 v162, v177, v162
	s_waitcnt lgkmcnt(3)
	v_mfma_f32_32x32x16_bf16 v[80:95], v[64:67], v[118:121], 0
	v_add_f32_e32 v162, v164, v162
	v_add_f32_e32 v162, v188, v162
	v_add_f32_e32 v162, v176, v162
	v_add_f32_e32 v162, v189, v162
	v_add_f32_e32 v162, v165, v162
	v_add_f32_e32 v162, v175, v162
	v_add_f32_e32 v162, v166, v162
	s_waitcnt lgkmcnt(2)
	v_mfma_f32_32x32x16_bf16 v[64:79], v[68:71], v[118:121], 0
	v_add_f32_e32 v162, v173, v162
	v_add_f32_e32 v162, v167, v162
	v_add_f32_e32 v162, v174, v162
	v_exp_f32_e32 v160, v160
	v_add_f32_e32 v162, v168, v162
	v_exp_f32_e32 v161, v161
	v_add_f32_e32 v162, v171, v162
	s_waitcnt lgkmcnt(1)
	v_mfma_f32_32x32x16_bf16 v[80:95], v[190:193], v[126:129], v[80:95]
	v_exp_f32_e32 v158, v158
	v_add_f32_e32 v162, v169, v162
	v_exp_f32_e32 v159, v159
	v_add_f32_e32 v162, v172, v162
	v_exp_f32_e32 v154, v154
	v_add_f32_e32 v162, v160, v162
	v_exp_f32_e32 v155, v155
	s_waitcnt lgkmcnt(0)
	v_mfma_f32_32x32x16_bf16 v[64:79], v[228:231], v[126:129], v[64:79]
	ds_read_b128 v[190:193], v222 offset:49152
	ds_read_b128 v[228:231], v222 offset:57344
	v_add_f32_e32 v162, v161, v162
	v_exp_f32_e32 v150, v150
	v_add_f32_e32 v162, v158, v162
	v_exp_f32_e32 v151, v151
	v_add_f32_e32 v162, v159, v162
	v_exp_f32_e32 v148, v148
	s_waitcnt lgkmcnt(1)
	v_mfma_f32_32x32x16_bf16 v[80:95], v[190:193], v[122:125], v[80:95]
	v_add_f32_e32 v162, v154, v162
	v_exp_f32_e32 v149, v149
	v_add_f32_e32 v162, v155, v162
	v_exp_f32_e32 v156, v156
	v_add_f32_e32 v162, v150, v162
	v_exp_f32_e32 v157, v157
	v_add_f32_e32 v162, v151, v162
	s_waitcnt lgkmcnt(0)
	v_mfma_f32_32x32x16_bf16 v[64:79], v[228:231], v[122:125], v[64:79]
	ds_read_b128 v[190:193], v210 offset:49152
	ds_read_b128 v[228:231], v210 offset:57344
	v_exp_f32_e32 v152, v152
	v_add_f32_e32 v162, v148, v162
	v_exp_f32_e32 v153, v153
	v_add_f32_e32 v162, v149, v162
	v_exp_f32_e32 v146, v146
	v_add_f32_e32 v162, v156, v162
	s_waitcnt lgkmcnt(1)
	v_mfma_f32_32x32x16_bf16 v[80:95], v[190:193], v[114:117], v[80:95]
	v_exp_f32_e32 v147, v147
	v_add_f32_e32 v162, v157, v162
	v_add_f32_e32 v162, v152, v162
	v_add_f32_e32 v162, v153, v162
	v_add_f32_e32 v162, v146, v162
	v_add_f32_e32 v227, v147, v162
	s_waitcnt lgkmcnt(0)
	v_mfma_f32_32x32x16_bf16 v[64:79], v[228:231], v[114:117], v[64:79]
	ds_read_b128 v[190:193], v211 offset:49152
	ds_read_b128 v[228:231], v211 offset:57344
	s_waitcnt lgkmcnt(1)
	v_mfma_f32_32x32x16_bf16 v[80:95], v[190:193], v[110:113], v[80:95]
	s_waitcnt lgkmcnt(0)
	v_mfma_f32_32x32x16_bf16 v[64:79], v[228:231], v[110:113], v[64:79]
	ds_read_b128 v[190:193], v223 offset:49152
	ds_read_b128 v[228:231], v223 offset:57344
	s_waitcnt lgkmcnt(1)
	v_mfma_f32_32x32x16_bf16 v[80:95], v[190:193], v[106:109], v[80:95]
	s_waitcnt lgkmcnt(0)
	v_mfma_f32_32x32x16_bf16 v[64:79], v[228:231], v[106:109], v[64:79]
	ds_read_b128 v[190:193], v225 offset:49152
	ds_read_b128 v[228:231], v225 offset:57344
	s_waitcnt lgkmcnt(1)
	v_mfma_f32_32x32x16_bf16 v[80:95], v[190:193], v[102:105], v[80:95]
	s_waitcnt lgkmcnt(0)
	v_mfma_f32_32x32x16_bf16 v[64:79], v[228:231], v[102:105], v[64:79]
	ds_read_b128 v[190:193], v224 offset:49152
	ds_read_b128 v[228:231], v224 offset:57344
	v_cvt_pk_bf16_f32 v162, v163, v177
	v_cvt_pk_bf16_f32 v163, v164, v188
	v_cvt_pk_bf16_f32 v164, v176, v189
	v_cvt_pk_bf16_f32 v165, v165, v175
	v_cvt_pk_bf16_f32 v166, v166, v173
	v_cvt_pk_bf16_f32 v167, v167, v174
	s_waitcnt lgkmcnt(1)
	v_mfma_f32_32x32x16_bf16 v[80:95], v[190:193], v[98:101], v[80:95]
	v_permlane32_swap_b32_e32 v162, v164
	v_cvt_pk_bf16_f32 v168, v168, v171
	v_cvt_pk_bf16_f32 v169, v169, v172
	v_cvt_pk_bf16_f32 v172, v160, v161
	v_cvt_pk_bf16_f32 v173, v158, v159
	v_cvt_pk_bf16_f32 v174, v154, v155
	s_waitcnt lgkmcnt(0)
	v_mfma_f32_32x32x16_bf16 v[64:79], v[228:231], v[98:101], v[64:79]
	v_mov_b32_e32 v228, v227
	s_nop 1
	v_permlane32_swap_b32_e32 v227, v228
	v_cvt_pk_bf16_f32 v175, v150, v151
	v_cvt_pk_bf16_f32 v230, v148, v149
	v_cvt_pk_bf16_f32 v231, v156, v157
	v_cvt_pk_bf16_f32 v232, v152, v153
	v_cvt_pk_bf16_f32 v233, v146, v147
	v_permlane32_swap_b32_e32 v163, v165
	v_permlane32_swap_b32_e32 v166, v168
	v_permlane32_swap_b32_e32 v167, v169
	v_permlane32_swap_b32_e32 v172, v174
	v_permlane32_swap_b32_e32 v173, v175
	v_permlane32_swap_b32_e32 v230, v232
	v_permlane32_swap_b32_e32 v231, v233
	ds_read_b64_tr_b16 v[234:235], v204 offset:0
	ds_read_b64_tr_b16 v[236:237], v204 offset:0x800
	ds_read_b64_tr_b16 v[238:239], v204 offset:0x1000
	ds_read_b64_tr_b16 v[240:241], v204 offset:0x1800
	ds_read_b64_tr_b16 v[242:243], v204 offset:0x2000
	ds_read_b64_tr_b16 v[244:245], v204 offset:0x2800
	ds_read_b64_tr_b16 v[246:247], v204 offset:0x3000
	ds_read_b64_tr_b16 v[248:249], v204 offset:0x3800
	s_waitcnt lgkmcnt(0)
	s_nop 0
	v_mfma_f32_32x32x16_bf16 v[0:15], v[162:165], v[234:237], v[0:15]
	ds_read_b64_tr_b16 v[234:235], v204 offset:0x200
	ds_read_b64_tr_b16 v[236:237], v204 offset:0xa00
	v_mfma_f32_32x32x16_bf16 v[0:15], v[166:169], v[238:241], v[0:15]
	ds_read_b64_tr_b16 v[238:239], v204 offset:0x1200
	ds_read_b64_tr_b16 v[240:241], v204 offset:0x1a00
	v_mfma_f32_32x32x16_bf16 v[0:15], v[172:175], v[242:245], v[0:15]
	ds_read_b64_tr_b16 v[242:243], v204 offset:0x2200
	ds_read_b64_tr_b16 v[244:245], v204 offset:0x2a00
	v_mfma_f32_32x32x16_bf16 v[0:15], v[230:233], v[246:249], v[0:15]
	ds_read_b64_tr_b16 v[246:247], v204 offset:0x3200
	ds_read_b64_tr_b16 v[248:249], v204 offset:0x3a00
	s_waitcnt lgkmcnt(0)
; #define SWRITE(b, i) do { *(LAS bf16x8*)(V_lds + (b) * SHM_V + vst0) = sr_[i].vs0;          \
;     *(LAS bf16x8*)(V_lds + (b) * SHM_V + vst1) = sr_[i].vs1; int kc = sc * 2;               \
;     *(LAS bf16x8*)(K_lds + (b) * SHM_K + KSWZ(sr, kc)) = sr_[i].ks0;                       \
;     *(LAS bf16x8*)(K_lds + (b) * SHM_K + KSWZ(32 + sr, kc)) = sr_[i].ks1; } while (0)
; #define SWAIT() asm volatile("s_waitcnt vmcnt(4)" ::: "memory")
; #define RESC(a) do { if (__any((a) < 1.f)) { if (hi == 0) al_l[r32] = (a); asm volatile("s_waitcnt lgkmcnt(0)" ::: "memory"); \
;     for (int d = 0; d < 4; ++d) for (int r = 0; r < 16; ++r) o[d][r] *= al_l[crow(r, hi)]; } } while (0)
; __device__ __forceinline__ void partialSM(f32x16& p0, f32x16& p1, float& m_reg, float& mn, float& alpha) {
;   constexpr float C = SCALE * 1.4426950408889634f;
;   float pmax = p0[0]; for (int r = 1; r < 16; ++r) pmax = fmaxf(pmax, p0[r]); for (int r = 0; r < 16; ++r) pmax = fmaxf(pmax, p1[r]);
;   { auto rr = __builtin_amdgcn_permlane32_swap(__float_as_uint(pmax), __float_as_uint(pmax), false, false);
;     pmax = fmaxf(__uint_as_float(rr[0]), __uint_as_float(rr[1])); }
;   if (__builtin_expect(__all(pmax - m_reg <= THR / SCALE), 1)) { mn = m_reg; alpha = 1.f; }
;   else { mn = fmaxf(m_reg, pmax); alpha = __builtin_amdgcn_exp2f((m_reg - mn) * C); m_reg = mn; }
; template <bool HALF> __device__ __forceinline__ void dense_body(const bf16_t* __restrict__ Qb, const bf16_t* __restrict__ Kh, const bf16_t* __restrict__ Vh, ...
;     ...
;     pv_d0(o, vb0, pa0, pa1, pa2, pa3); partialSM(pB0, pB1, m_reg, mnB, alB);
;     __syncthreads(); SWAIT(); SWRITE(0, SE);
;     RESC(alB); __syncthreads();
	v_mfma_f32_32x32x16_bf16 v[48:63], v[162:165], v[234:237], v[48:63]
	ds_read_b64_tr_b16 v[234:235], v204 offset:0x400
	ds_read_b64_tr_b16 v[236:237], v204 offset:0xc00
	v_mfma_f32_32x32x16_bf16 v[48:63], v[166:169], v[238:241], v[48:63]
	ds_read_b64_tr_b16 v[238:239], v204 offset:0x1400
	ds_read_b64_tr_b16 v[240:241], v204 offset:0x1c00
	v_mfma_f32_32x32x16_bf16 v[48:63], v[172:175], v[242:245], v[48:63]
	ds_read_b64_tr_b16 v[242:243], v204 offset:0x2400
	ds_read_b64_tr_b16 v[244:245], v204 offset:0x2c00
	v_mfma_f32_32x32x16_bf16 v[48:63], v[230:233], v[246:249], v[48:63]
	ds_read_b64_tr_b16 v[246:247], v204 offset:0x3400
	ds_read_b64_tr_b16 v[248:249], v204 offset:0x3c00
	s_waitcnt lgkmcnt(0)
	v_mfma_f32_32x32x16_bf16 v[32:47], v[162:165], v[234:237], v[32:47]
	ds_read_b64_tr_b16 v[234:235], v204 offset:0x600
	ds_read_b64_tr_b16 v[236:237], v204 offset:0xe00
	v_mfma_f32_32x32x16_bf16 v[32:47], v[166:169], v[238:241], v[32:47]
	ds_read_b64_tr_b16 v[238:239], v204 offset:0x1600
	ds_read_b64_tr_b16 v[240:241], v204 offset:0x1e00
	v_mfma_f32_32x32x16_bf16 v[32:47], v[172:175], v[242:245], v[32:47]
	ds_read_b64_tr_b16 v[242:243], v204 offset:0x2600
	ds_read_b64_tr_b16 v[244:245], v204 offset:0x2e00
	v_mfma_f32_32x32x16_bf16 v[32:47], v[230:233], v[246:249], v[32:47]
	ds_read_b64_tr_b16 v[246:247], v204 offset:0x3600
	ds_read_b64_tr_b16 v[248:249], v204 offset:0x3e00
	s_waitcnt lgkmcnt(0)
	v_mfma_f32_32x32x16_bf16 v[16:31], v[162:165], v[234:237], v[16:31]
	v_max_f32_e32 v162, v81, v81
	v_max_f32_e32 v163, v80, v80
	v_max_f32_e32 v162, v163, v162
	v_max3_f32 v162, v162, v82, v83
	v_max3_f32 v162, v162, v84, v85
	v_max3_f32 v162, v162, v86, v87
	v_max3_f32 v162, v162, v88, v89
	v_max3_f32 v162, v162, v90, v91
	v_max3_f32 v162, v162, v92, v93
	v_mfma_f32_32x32x16_bf16 v[16:31], v[166:169], v[238:241], v[16:31]
	v_max3_f32 v162, v162, v94, v95
	v_max3_f32 v162, v162, v64, v65
	v_max3_f32 v162, v162, v66, v67
	v_max3_f32 v162, v162, v68, v69
	v_max3_f32 v162, v162, v70, v71
	v_max3_f32 v162, v162, v72, v73
	v_max3_f32 v162, v162, v74, v75
	v_max3_f32 v162, v162, v76, v77
	v_mfma_f32_32x32x16_bf16 v[16:31], v[172:175], v[242:245], v[16:31]
	v_max3_f32 v162, v162, v78, v79
	v_mov_b32_e32 v163, v162
	s_nop 1
	v_permlane32_swap_b32_e32 v162, v163
	v_max_f32_e32 v163, v163, v163
	v_max_f32_e32 v162, v162, v162
	v_max_f32_e32 v162, v162, v163
	v_sub_f32_e32 v163, v162, v170
	v_cmp_ge_f32_e32 vcc, s87, v163
	v_max_f32_e32 v163, v170, v170
	v_max_f32_e32 v162, v163, v162
	v_mfma_f32_32x32x16_bf16 v[16:31], v[230:233], v[246:249], v[16:31]
	v_sub_f32_e32 v163, v170, v162
	v_mul_f32_e32 v163, 0x3e0293ee, v163
	v_exp_f32_e32 v163, v163
	s_cmp_eq_u64 vcc, exec
	s_cselect_b64 s[42:43], -1, 0
	s_waitcnt vmcnt(0)
	s_barrier
	s_add_i32 m0, s52, 0x4000
	s_nop 0
	global_load_lds_dwordx4 v130, s[48:49]
	s_add_i32 m0, s52, 0x4400
	s_nop 0
	global_load_lds_dwordx4 v131, s[48:49]
	s_add_i32 m0, s53, 0x0
	s_nop 0
	global_load_lds_dwordx4 v132, s[50:51]
	s_add_i32 m0, s53, 0x400
	s_nop 0
	global_load_lds_dwordx4 v133, s[50:51]
	s_add_u32 s48, s48, 0x18000
	s_addc_u32 s49, s49, 0
	s_add_u32 s50, s50, 0xc0000
	s_addc_u32 s51, s51, 0
	v_cndmask_b32_e64 v229, v163, 1.0, s[42:43]
	v_cmp_gt_f32_e32 vcc, 1.0, v229
	s_cbranch_vccz .LBB0_429
	s_and_saveexec_b64 s[6:7], s[40:41]
	ds_write_b32 v201, v229 offset:128
	s_or_b64 exec, exec, s[6:7]
	s_waitcnt lgkmcnt(0)
	v_add_u32_e32 v163, v200, v96
	ds_read_b128 v[164:167], v163 offset:224
	ds_read_b128 v[172:175], v163 offset:192
	ds_read_b128 v[230:233], v163 offset:160
	ds_read_b128 v[234:237], v163 offset:128
	s_waitcnt lgkmcnt(3)
	v_pk_mul_f32 v[12:13], v[12:13], v[164:165]
	s_waitcnt lgkmcnt(2)
	v_pk_mul_f32 v[8:9], v[8:9], v[172:173]
	s_waitcnt lgkmcnt(1)
	v_pk_mul_f32 v[4:5], v[4:5], v[230:231]
	v_pk_mul_f32 v[14:15], v[14:15], v[166:167]
	v_pk_mul_f32 v[10:11], v[10:11], v[174:175]
	v_pk_mul_f32 v[6:7], v[6:7], v[232:233]
	s_waitcnt lgkmcnt(0)
	v_pk_mul_f32 v[2:3], v[2:3], v[236:237]
	v_pk_mul_f32 v[0:1], v[0:1], v[234:235]
	v_pk_mul_f32 v[60:61], v[60:61], v[164:165]
	v_pk_mul_f32 v[56:57], v[56:57], v[172:173]
	v_pk_mul_f32 v[52:53], v[52:53], v[230:231]
	v_pk_mul_f32 v[62:63], v[62:63], v[166:167]
	v_pk_mul_f32 v[58:59], v[58:59], v[174:175]
	v_pk_mul_f32 v[54:55], v[54:55], v[232:233]
	v_pk_mul_f32 v[50:51], v[50:51], v[236:237]
	v_pk_mul_f32 v[48:49], v[48:49], v[234:235]
	v_pk_mul_f32 v[44:45], v[44:45], v[164:165]
	v_pk_mul_f32 v[40:41], v[40:41], v[172:173]
	v_pk_mul_f32 v[36:37], v[36:37], v[230:231]
	v_pk_mul_f32 v[46:47], v[46:47], v[166:167]
	v_pk_mul_f32 v[42:43], v[42:43], v[174:175]
	v_pk_mul_f32 v[38:39], v[38:39], v[232:233]
	v_pk_mul_f32 v[34:35], v[34:35], v[236:237]
	v_pk_mul_f32 v[32:33], v[32:33], v[234:235]
	v_pk_mul_f32 v[28:29], v[28:29], v[164:165]
	v_pk_mul_f32 v[24:25], v[24:25], v[172:173]
	v_pk_mul_f32 v[20:21], v[20:21], v[230:231]
	v_pk_mul_f32 v[30:31], v[30:31], v[166:167]
	v_pk_mul_f32 v[26:27], v[26:27], v[174:175]
	v_pk_mul_f32 v[22:23], v[22:23], v[232:233]
	v_pk_mul_f32 v[18:19], v[18:19], v[236:237]
	v_pk_mul_f32 v[16:17], v[16:17], v[234:235]
; #define SBAR() __builtin_amdgcn_sched_barrier(0)
; #define RESC(a) do { if (__any((a) < 1.f)) { if (hi == 0) al_l[r32] = (a); asm volatile("s_waitcnt lgkmcnt(0)" ::: "memory"); \
;     for (int d = 0; d < 4; ++d) for (int r = 0; r < 16; ++r) o[d][r] *= al_l[crow(r, hi)]; } } while (0)
; __device__ __forceinline__ void partialSM(f32x16& p0, f32x16& p1, float& m_reg, float& mn, float& alpha) {
;     ...
;   else { mn = fmaxf(m_reg, pmax); alpha = __builtin_amdgcn_exp2f((m_reg - mn) * C); m_reg = mn; }
;   float mnC = -mn * C;
;   for (int r = 0; r < 16; ++r) p0[r] = fmaf(p0[r], C, mnC); for (int r = 0; r < 16; ++r) p1[r] = fmaf(p1[r], C, mnC);
;   for (int r = 0; r < 16; ++r) p0[r] = __builtin_amdgcn_exp2f(p0[r]);
; }
; __device__ __forceinline__ void finishSM(f32x16& p0, f32x16& p1, float alpha, float& l_reg, bf16x8& pa0, bf16x8& pa1, bf16x8& pa2, bf16x8& pa3) {
;   for (int r = 0; r < 16; ++r) p1[r] = __builtin_amdgcn_exp2f(p1[r]);
;   float ps = 0; for (int r = 0; r < 16; ++r) ps += p0[r]; for (int r = 0; r < 16; ++r) ps += p1[r];
;   { auto rr = __builtin_amdgcn_permlane32_swap(__float_as_uint(ps), __float_as_uint(ps), false, false);
;     ps = __uint_as_float(rr[0]) + __uint_as_float(rr[1]); }
;   l_reg = l_reg * alpha + ps;
;     ...
;   PK4(p0, 0, pa0); PK4(p0, 8, pa1); PK4(p1, 0, pa2); PK4(p1, 8, pa3);
;     ...
; }
; template <bool HALF> __device__ __forceinline__ void qkt(f32x16& p0, f32x16& p1, const char* Ks, const bf16x8* qr, int r32, int hi, int koff) {
;   p0 = f32x16{}; p1 = f32x16{};
;   for (int d0 = 0; d0 < (HALF ? 4 : 8); ++d0) { int cb = (d0 * 16 + hi * 8) * 2 + koff;
;     bf16x8 b0 = *reinterpret_cast<const bf16x8*>(Ks + KSWZ(r32, cb));
;     bf16x8 b1 = *reinterpret_cast<const bf16x8*>(Ks + KSWZ(32 + r32, cb));
;     p0 = __builtin_amdgcn_mfma_f32_32x32x16_bf16(b0, qr[d0], p0, 0, 0, 0);
;     p1 = __builtin_amdgcn_mfma_f32_32x32x16_bf16(b1, qr[d0], p1, 0, 0, 0); }
; template <bool HALF> __device__ __forceinline__ void dense_body(const bf16_t* __restrict__ Qb, const bf16_t* __restrict__ Kh, const bf16_t* __restrict__ Vh, ...
;     ...
;     RESC(alB); __syncthreads();
;     SBAR(); qkt<HALF>(pA0, pA1, Kl0, qr, r32, hi, koff);
;     finishSM(pB0, pB1, alB, l_reg, pa0, pa1, pa2, pa3); SBAR();
;     if (j + 3 < NT) SLOAD(SE, (j + 3) * KVBLK); SBAR();
.LBB0_429:
	v_cndmask_b32_e64 v230, v162, v170, s[42:43]
	v_mul_f32_e32 v231, 0xbe0293ee, v230
	v_fmamk_f32 v80, v80, 0x3e0293ee, v231
	v_fmamk_f32 v81, v81, 0x3e0293ee, v231
	v_fmamk_f32 v82, v82, 0x3e0293ee, v231
	v_fmamk_f32 v83, v83, 0x3e0293ee, v231
	v_fmamk_f32 v84, v84, 0x3e0293ee, v231
	v_fmamk_f32 v85, v85, 0x3e0293ee, v231
	v_fmamk_f32 v86, v86, 0x3e0293ee, v231
	v_fmamk_f32 v87, v87, 0x3e0293ee, v231
	v_fmamk_f32 v88, v88, 0x3e0293ee, v231
	v_fmamk_f32 v89, v89, 0x3e0293ee, v231
	v_fmamk_f32 v90, v90, 0x3e0293ee, v231
	v_fmamk_f32 v91, v91, 0x3e0293ee, v231
	v_fmamk_f32 v92, v92, 0x3e0293ee, v231
	v_fmamk_f32 v93, v93, 0x3e0293ee, v231
	v_fmamk_f32 v94, v94, 0x3e0293ee, v231
	v_fmamk_f32 v95, v95, 0x3e0293ee, v231
	v_exp_f32_e32 v162, v80
	v_exp_f32_e32 v177, v81
	v_exp_f32_e32 v163, v82
	v_exp_f32_e32 v176, v83
	v_exp_f32_e32 v164, v84
	v_exp_f32_e32 v175, v85
	v_exp_f32_e32 v165, v86
	v_exp_f32_e32 v174, v87
	v_exp_f32_e32 v166, v88
	v_exp_f32_e32 v173, v89
	v_exp_f32_e32 v167, v90
	v_exp_f32_e32 v172, v91
	v_exp_f32_e32 v168, v92
	v_exp_f32_e32 v171, v93
	v_exp_f32_e32 v169, v94
	v_exp_f32_e32 v170, v95
	v_fmamk_f32 v240, v64, 0x3e0293ee, v231
	v_fmamk_f32 v241, v65, 0x3e0293ee, v231
	v_fmamk_f32 v242, v66, 0x3e0293ee, v231
	v_fmamk_f32 v243, v67, 0x3e0293ee, v231
	v_fmamk_f32 v244, v68, 0x3e0293ee, v231
	v_fmamk_f32 v233, v69, 0x3e0293ee, v231
	v_fmamk_f32 v234, v70, 0x3e0293ee, v231
	v_fmamk_f32 v235, v71, 0x3e0293ee, v231
	v_fmamk_f32 v236, v72, 0x3e0293ee, v231
	v_fmamk_f32 v237, v73, 0x3e0293ee, v231
	v_fmamk_f32 v238, v74, 0x3e0293ee, v231
	v_fmamk_f32 v239, v75, 0x3e0293ee, v231
	v_fmamk_f32 v232, v76, 0x3e0293ee, v231
	v_fmamk_f32 v245, v77, 0x3e0293ee, v231
	v_fmamk_f32 v246, v78, 0x3e0293ee, v231
	v_fmac_f32_e32 v231, 0x3e0293ee, v79
	s_waitcnt lgkmcnt(0)
	ds_read_b128 v[64:67], v209 offset:32768
	ds_read_b128 v[68:71], v209 offset:40960
	ds_read_b128 v[248:251], v221 offset:32768
	ds_read_b128 v[212:215], v221 offset:40960
	v_exp_f32_e32 v233, v233
	v_exp_f32_e32 v234, v234
	s_waitcnt lgkmcnt(3)
	v_mfma_f32_32x32x16_bf16 v[80:95], v[64:67], v[118:121], 0
	v_exp_f32_e32 v235, v235
	v_exp_f32_e32 v236, v236
	v_exp_f32_e32 v237, v237
	v_exp_f32_e32 v238, v238
	v_exp_f32_e32 v239, v239
	s_waitcnt lgkmcnt(2)
	v_mfma_f32_32x32x16_bf16 v[64:79], v[68:71], v[118:121], 0
	s_waitcnt lgkmcnt(1)
	v_mfma_f32_32x32x16_bf16 v[80:95], v[248:251], v[126:129], v[80:95]
	s_waitcnt lgkmcnt(0)
	v_mfma_f32_32x32x16_bf16 v[64:79], v[212:215], v[126:129], v[64:79]
	ds_read_b128 v[212:215], v222 offset:32768
	ds_read_b128 v[248:251], v222 offset:40960
	s_waitcnt lgkmcnt(1)
	v_mfma_f32_32x32x16_bf16 v[80:95], v[212:215], v[122:125], v[80:95]
	s_waitcnt lgkmcnt(0)
	v_mfma_f32_32x32x16_bf16 v[64:79], v[248:251], v[122:125], v[64:79]
	ds_read_b128 v[212:215], v210 offset:32768
	ds_read_b128 v[248:251], v210 offset:40960
	s_waitcnt lgkmcnt(1)
	v_mfma_f32_32x32x16_bf16 v[80:95], v[212:215], v[114:117], v[80:95]
	s_waitcnt lgkmcnt(0)
	v_mfma_f32_32x32x16_bf16 v[64:79], v[248:251], v[114:117], v[64:79]
	ds_read_b128 v[212:215], v211 offset:32768
	ds_read_b128 v[248:251], v211 offset:40960
	s_waitcnt lgkmcnt(1)
	v_mfma_f32_32x32x16_bf16 v[80:95], v[212:215], v[110:113], v[80:95]
	s_waitcnt lgkmcnt(0)
	v_mfma_f32_32x32x16_bf16 v[64:79], v[248:251], v[110:113], v[64:79]
	ds_read_b128 v[212:215], v223 offset:32768
	ds_read_b128 v[248:251], v223 offset:40960
	s_waitcnt lgkmcnt(1)
	v_mfma_f32_32x32x16_bf16 v[80:95], v[212:215], v[106:109], v[80:95]
	s_waitcnt lgkmcnt(0)
	v_mfma_f32_32x32x16_bf16 v[64:79], v[248:251], v[106:109], v[64:79]
	ds_read_b128 v[212:215], v225 offset:32768
	ds_read_b128 v[248:251], v225 offset:40960
	s_waitcnt lgkmcnt(1)
	v_mfma_f32_32x32x16_bf16 v[80:95], v[212:215], v[102:105], v[80:95]
	s_waitcnt lgkmcnt(0)
	v_mfma_f32_32x32x16_bf16 v[64:79], v[248:251], v[102:105], v[64:79]
	ds_read_b128 v[212:215], v224 offset:32768
	ds_read_b128 v[248:251], v224 offset:40960
	s_waitcnt lgkmcnt(1)
	v_mfma_f32_32x32x16_bf16 v[80:95], v[212:215], v[98:101], v[80:95]
	v_exp_f32_e32 v212, v240
	v_exp_f32_e32 v240, v244
	v_exp_f32_e32 v244, v231
	v_add_f32_e32 v231, 0, v162
	v_add_f32_e32 v231, v177, v231
	v_add_f32_e32 v231, v163, v231
	v_add_f32_e32 v231, v176, v231
	v_add_f32_e32 v231, v164, v231
	v_add_f32_e32 v231, v175, v231
	v_add_f32_e32 v231, v165, v231
	v_add_f32_e32 v231, v174, v231
	v_add_f32_e32 v231, v166, v231
	v_add_f32_e32 v231, v173, v231
	v_add_f32_e32 v231, v167, v231
	v_add_f32_e32 v231, v172, v231
	v_add_f32_e32 v231, v168, v231
	v_exp_f32_e32 v213, v241
	v_add_f32_e32 v231, v171, v231
	v_exp_f32_e32 v214, v242
	v_add_f32_e32 v231, v169, v231
	v_exp_f32_e32 v215, v243
	v_add_f32_e32 v231, v170, v231
	v_add_f32_e32 v231, v212, v231
	v_add_f32_e32 v231, v213, v231
	v_add_f32_e32 v231, v214, v231
	v_add_f32_e32 v231, v215, v231
	v_add_f32_e32 v231, v240, v231
	v_add_f32_e32 v231, v233, v231
	v_add_f32_e32 v231, v234, v231
	v_add_f32_e32 v231, v235, v231
	v_exp_f32_e32 v241, v232
	v_add_f32_e32 v231, v236, v231
	v_exp_f32_e32 v242, v245
	v_add_f32_e32 v231, v237, v231
	s_waitcnt lgkmcnt(0)
	v_mfma_f32_32x32x16_bf16 v[64:79], v[248:251], v[98:101], v[64:79]
	v_exp_f32_e32 v243, v246
	v_add_f32_e32 v231, v238, v231
	v_add_f32_e32 v231, v239, v231
	v_add_f32_e32 v231, v241, v231
	v_add_f32_e32 v231, v242, v231
	v_add_f32_e32 v231, v243, v231
	v_add_f32_e32 v231, v244, v231
	v_mov_b32_e32 v232, v231
	v_cvt_pk_bf16_f32 v162, v162, v177
	v_cvt_pk_bf16_f32 v163, v163, v176
	v_cvt_pk_bf16_f32 v164, v164, v175
	v_cvt_pk_bf16_f32 v165, v165, v174
	v_cvt_pk_bf16_f32 v166, v166, v173
	v_cvt_pk_bf16_f32 v167, v167, v172
	v_cvt_pk_bf16_f32 v168, v168, v171
	v_cvt_pk_bf16_f32 v169, v169, v170
	v_cvt_pk_bf16_f32 v170, v212, v213
	v_cvt_pk_bf16_f32 v171, v214, v215
	v_cvt_pk_bf16_f32 v172, v240, v233
	v_cvt_pk_bf16_f32 v173, v234, v235
	v_cvt_pk_bf16_f32 v174, v236, v237
	v_cvt_pk_bf16_f32 v175, v238, v239
	v_cvt_pk_bf16_f32 v176, v241, v242
	v_cvt_pk_bf16_f32 v177, v243, v244
	s_nop 1
	v_permlane32_swap_b32_e32 v231, v232
	v_permlane32_swap_b32_e32 v162, v164
	v_permlane32_swap_b32_e32 v163, v165
	v_permlane32_swap_b32_e32 v166, v168
	v_permlane32_swap_b32_e32 v167, v169
	v_permlane32_swap_b32_e32 v170, v172
	v_permlane32_swap_b32_e32 v171, v173
	v_permlane32_swap_b32_e32 v174, v176
	v_permlane32_swap_b32_e32 v175, v177
	s_cmp_ge_u32 s2, s4
	s_cselect_b64 s[20:21], -1, 0
; #define SBAR() __builtin_amdgcn_sched_barrier(0)
; #define SWRITE(b, i) do { *(LAS bf16x8*)(V_lds + (b) * SHM_V + vst0) = sr_[i].vs0;          \
;     *(LAS bf16x8*)(V_lds + (b) * SHM_V + vst1) = sr_[i].vs1; int kc = sc * 2;               \
;     *(LAS bf16x8*)(K_lds + (b) * SHM_K + KSWZ(sr, kc)) = sr_[i].ks0;                       \
;     *(LAS bf16x8*)(K_lds + (b) * SHM_K + KSWZ(32 + sr, kc)) = sr_[i].ks1; } while (0)
; #define SWAIT() asm volatile("s_waitcnt vmcnt(4)" ::: "memory")
; #define RESC(a) do { if (__any((a) < 1.f)) { if (hi == 0) al_l[r32] = (a); asm volatile("s_waitcnt lgkmcnt(0)" ::: "memory"); \
;     for (int d = 0; d < 4; ++d) for (int r = 0; r < 16; ++r) o[d][r] *= al_l[crow(r, hi)]; } } while (0)
; __device__ __forceinline__ void partialSM(f32x16& p0, f32x16& p1, float& m_reg, float& mn, float& alpha) {
;   constexpr float C = SCALE * 1.4426950408889634f;
;   float pmax = p0[0]; for (int r = 1; r < 16; ++r) pmax = fmaxf(pmax, p0[r]); for (int r = 0; r < 16; ++r) pmax = fmaxf(pmax, p1[r]);
;   { auto rr = __builtin_amdgcn_permlane32_swap(__float_as_uint(pmax), __float_as_uint(pmax), false, false);
;     pmax = fmaxf(__uint_as_float(rr[0]), __uint_as_float(rr[1])); }
;   if (__builtin_expect(__all(pmax - m_reg <= THR / SCALE), 1)) { mn = m_reg; alpha = 1.f; }
;   else { mn = fmaxf(m_reg, pmax); alpha = __builtin_amdgcn_exp2f((m_reg - mn) * C); m_reg = mn; }
; template <bool HALF> __device__ __forceinline__ void dense_body(const bf16_t* __restrict__ Qb, const bf16_t* __restrict__ Kh, const bf16_t* __restrict__ Vh, ...
;     ...
;     if (j + 3 < NT) SLOAD(SE, (j + 3) * KVBLK); SBAR();
;     pv_d0(o, vb0 + (int)SHM_V, pa0, pa1, pa2, pa3); partialSM(pA0, pA1, m_reg, mnA, alA);
;     __syncthreads(); SWAIT(); SWRITE(1, SO);
;     RESC(alA); __syncthreads();
.LBB0_431:
	ds_read_b64_tr_b16 v[188:189], v203 offset:0
	ds_read_b64_tr_b16 v[190:191], v203 offset:0x800
	ds_read_b64_tr_b16 v[192:193], v203 offset:0x1000
	ds_read_b64_tr_b16 v[194:195], v203 offset:0x1800
	ds_read_b64_tr_b16 v[212:213], v203 offset:0x2000
	ds_read_b64_tr_b16 v[214:215], v203 offset:0x2800
	ds_read_b64_tr_b16 v[234:235], v203 offset:0x3000
	ds_read_b64_tr_b16 v[236:237], v203 offset:0x3800
	s_waitcnt lgkmcnt(0)
	s_nop 0
	v_mfma_f32_32x32x16_bf16 v[0:15], v[162:165], v[188:191], v[0:15]
	ds_read_b64_tr_b16 v[188:189], v203 offset:0x200
	ds_read_b64_tr_b16 v[190:191], v203 offset:0xa00
	v_mfma_f32_32x32x16_bf16 v[0:15], v[166:169], v[192:195], v[0:15]
	ds_read_b64_tr_b16 v[192:193], v203 offset:0x1200
	ds_read_b64_tr_b16 v[194:195], v203 offset:0x1a00
	v_mfma_f32_32x32x16_bf16 v[0:15], v[170:173], v[212:215], v[0:15]
	ds_read_b64_tr_b16 v[212:213], v203 offset:0x2200
	ds_read_b64_tr_b16 v[214:215], v203 offset:0x2a00
	v_mfma_f32_32x32x16_bf16 v[0:15], v[174:177], v[234:237], v[0:15]
	ds_read_b64_tr_b16 v[234:235], v203 offset:0x3200
	ds_read_b64_tr_b16 v[236:237], v203 offset:0x3a00
	s_waitcnt lgkmcnt(0)
	v_mfma_f32_32x32x16_bf16 v[48:63], v[162:165], v[188:191], v[48:63]
	ds_read_b64_tr_b16 v[188:189], v203 offset:0x400
	ds_read_b64_tr_b16 v[190:191], v203 offset:0xc00
	v_mfma_f32_32x32x16_bf16 v[48:63], v[166:169], v[192:195], v[48:63]
	ds_read_b64_tr_b16 v[192:193], v203 offset:0x1400
	ds_read_b64_tr_b16 v[194:195], v203 offset:0x1c00
	v_mfma_f32_32x32x16_bf16 v[48:63], v[170:173], v[212:215], v[48:63]
	ds_read_b64_tr_b16 v[212:213], v203 offset:0x2400
	ds_read_b64_tr_b16 v[214:215], v203 offset:0x2c00
	v_mfma_f32_32x32x16_bf16 v[48:63], v[174:177], v[234:237], v[48:63]
	ds_read_b64_tr_b16 v[234:235], v203 offset:0x3400
	ds_read_b64_tr_b16 v[236:237], v203 offset:0x3c00
	s_waitcnt lgkmcnt(0)
	v_mfma_f32_32x32x16_bf16 v[32:47], v[162:165], v[188:191], v[32:47]
	ds_read_b64_tr_b16 v[188:189], v203 offset:0x600
	ds_read_b64_tr_b16 v[190:191], v203 offset:0xe00
	v_mfma_f32_32x32x16_bf16 v[32:47], v[166:169], v[192:195], v[32:47]
	ds_read_b64_tr_b16 v[192:193], v203 offset:0x1600
	ds_read_b64_tr_b16 v[194:195], v203 offset:0x1e00
	v_mfma_f32_32x32x16_bf16 v[32:47], v[170:173], v[212:215], v[32:47]
	ds_read_b64_tr_b16 v[212:213], v203 offset:0x2600
	ds_read_b64_tr_b16 v[214:215], v203 offset:0x2e00
	v_mfma_f32_32x32x16_bf16 v[32:47], v[174:177], v[234:237], v[32:47]
	ds_read_b64_tr_b16 v[234:235], v203 offset:0x3600
	ds_read_b64_tr_b16 v[236:237], v203 offset:0x3e00
	s_waitcnt lgkmcnt(0)
	v_mfma_f32_32x32x16_bf16 v[16:31], v[162:165], v[188:191], v[16:31]
	v_max_f32_e32 v162, v81, v81
	v_max_f32_e32 v163, v80, v80
	v_max_f32_e32 v162, v163, v162
	v_max3_f32 v162, v162, v82, v83
	v_max3_f32 v162, v162, v84, v85
	v_max3_f32 v162, v162, v86, v87
	v_max3_f32 v162, v162, v88, v89
	v_max3_f32 v162, v162, v90, v91
	v_max3_f32 v162, v162, v92, v93
	v_mfma_f32_32x32x16_bf16 v[16:31], v[166:169], v[192:195], v[16:31]
	v_max3_f32 v162, v162, v94, v95
	v_max3_f32 v162, v162, v64, v65
	v_max3_f32 v162, v162, v66, v67
	v_max3_f32 v162, v162, v68, v69
	v_max3_f32 v162, v162, v70, v71
	v_max3_f32 v162, v162, v72, v73
	v_max3_f32 v162, v162, v74, v75
	v_max3_f32 v162, v162, v76, v77
	v_mfma_f32_32x32x16_bf16 v[16:31], v[170:173], v[212:215], v[16:31]
	v_max3_f32 v162, v162, v78, v79
	v_mov_b32_e32 v163, v162
	s_nop 1
	v_permlane32_swap_b32_e32 v162, v163
	v_max_f32_e32 v163, v163, v163
	v_max_f32_e32 v162, v162, v162
	v_max_f32_e32 v162, v162, v163
	v_sub_f32_e32 v163, v162, v230
	v_cmp_ge_f32_e32 vcc, s87, v163
	v_max_f32_e32 v163, v230, v230
	v_max_f32_e32 v163, v163, v162
	v_mfma_f32_32x32x16_bf16 v[16:31], v[174:177], v[234:237], v[16:31]
	v_sub_f32_e32 v162, v230, v163
	v_mul_f32_e32 v162, 0x3e0293ee, v162
	v_exp_f32_e32 v162, v162
	s_cmp_eq_u64 vcc, exec
	s_cselect_b64 s[42:43], -1, 0
	s_waitcnt vmcnt(0)
	s_barrier
	s_add_i32 m0, s52, 0x0
	s_nop 0
	global_load_lds_dwordx4 v130, s[48:49]
	s_add_i32 m0, s52, 0x400
	s_nop 0
	global_load_lds_dwordx4 v131, s[48:49]
	s_add_i32 m0, s53, 0x4000
	s_nop 0
	global_load_lds_dwordx4 v132, s[50:51]
	s_add_i32 m0, s53, 0x4400
	s_nop 0
	global_load_lds_dwordx4 v133, s[50:51]
	s_add_u32 s48, s48, 0x18000
	s_addc_u32 s49, s49, 0
	s_add_u32 s50, s50, 0xc0000
	s_addc_u32 s51, s51, 0
	v_cndmask_b32_e64 v162, v162, 1.0, s[42:43]
	v_cmp_gt_f32_e32 vcc, 1.0, v162
	s_cbranch_vccz .LBB0_435
	s_and_saveexec_b64 s[6:7], s[40:41]
	ds_write_b32 v201, v162 offset:128
	s_or_b64 exec, exec, s[6:7]
	s_waitcnt lgkmcnt(0)
	v_add_u32_e32 v158, v200, v96
	ds_read_b128 v[146:149], v158 offset:224
	ds_read_b128 v[150:153], v158 offset:192
	ds_read_b128 v[154:157], v158 offset:160
	ds_read_b128 v[158:161], v158 offset:128
	s_waitcnt lgkmcnt(3)
	v_pk_mul_f32 v[12:13], v[12:13], v[146:147]
	s_waitcnt lgkmcnt(2)
	v_pk_mul_f32 v[8:9], v[8:9], v[150:151]
	s_waitcnt lgkmcnt(1)
	v_pk_mul_f32 v[4:5], v[4:5], v[154:155]
	v_pk_mul_f32 v[14:15], v[14:15], v[148:149]
	v_pk_mul_f32 v[10:11], v[10:11], v[152:153]
	v_pk_mul_f32 v[6:7], v[6:7], v[156:157]
	s_waitcnt lgkmcnt(0)
	v_pk_mul_f32 v[2:3], v[2:3], v[160:161]
	v_pk_mul_f32 v[0:1], v[0:1], v[158:159]
	v_pk_mul_f32 v[60:61], v[60:61], v[146:147]
	v_pk_mul_f32 v[56:57], v[56:57], v[150:151]
	v_pk_mul_f32 v[52:53], v[52:53], v[154:155]
	v_pk_mul_f32 v[62:63], v[62:63], v[148:149]
	v_pk_mul_f32 v[58:59], v[58:59], v[152:153]
	v_pk_mul_f32 v[54:55], v[54:55], v[156:157]
	v_pk_mul_f32 v[50:51], v[50:51], v[160:161]
	v_pk_mul_f32 v[48:49], v[48:49], v[158:159]
	v_pk_mul_f32 v[44:45], v[44:45], v[146:147]
	v_pk_mul_f32 v[40:41], v[40:41], v[150:151]
	v_pk_mul_f32 v[36:37], v[36:37], v[154:155]
	v_pk_mul_f32 v[46:47], v[46:47], v[148:149]
	v_pk_mul_f32 v[42:43], v[42:43], v[152:153]
	v_pk_mul_f32 v[38:39], v[38:39], v[156:157]
	v_pk_mul_f32 v[34:35], v[34:35], v[160:161]
	v_pk_mul_f32 v[32:33], v[32:33], v[158:159]
	v_pk_mul_f32 v[28:29], v[28:29], v[146:147]
	v_pk_mul_f32 v[24:25], v[24:25], v[150:151]
	v_pk_mul_f32 v[20:21], v[20:21], v[154:155]
	v_pk_mul_f32 v[30:31], v[30:31], v[148:149]
	v_pk_mul_f32 v[26:27], v[26:27], v[152:153]
	v_pk_mul_f32 v[22:23], v[22:23], v[156:157]
	v_pk_mul_f32 v[18:19], v[18:19], v[160:161]
	v_pk_mul_f32 v[16:17], v[16:17], v[158:159]
; #define SBAR() __builtin_amdgcn_sched_barrier(0)
; #define SWRITE(b, i) do { *(LAS bf16x8*)(V_lds + (b) * SHM_V + vst0) = sr_[i].vs0;          \
;     *(LAS bf16x8*)(V_lds + (b) * SHM_V + vst1) = sr_[i].vs1; int kc = sc * 2;               \
;     *(LAS bf16x8*)(K_lds + (b) * SHM_K + KSWZ(sr, kc)) = sr_[i].ks0;                       \
;     *(LAS bf16x8*)(K_lds + (b) * SHM_K + KSWZ(32 + sr, kc)) = sr_[i].ks1; } while (0)
; #define SWAIT() asm volatile("s_waitcnt vmcnt(4)" ::: "memory")
; #define RESC(a) do { if (__any((a) < 1.f)) { if (hi == 0) al_l[r32] = (a); asm volatile("s_waitcnt lgkmcnt(0)" ::: "memory"); \
;     for (int d = 0; d < 4; ++d) for (int r = 0; r < 16; ++r) o[d][r] *= al_l[crow(r, hi)]; } } while (0)
; __device__ __forceinline__ void partialSM(f32x16& p0, f32x16& p1, float& m_reg, float& mn, float& alpha) {
;     ...
;   float mnC = -mn * C;
;   for (int r = 0; r < 16; ++r) p0[r] = fmaf(p0[r], C, mnC); for (int r = 0; r < 16; ++r) p1[r] = fmaf(p1[r], C, mnC);
;   for (int r = 0; r < 16; ++r) p0[r] = __builtin_amdgcn_exp2f(p0[r]);
; }
; __device__ __forceinline__ void finishSM(f32x16& p0, f32x16& p1, float alpha, float& l_reg, bf16x8& pa0, bf16x8& pa1, bf16x8& pa2, bf16x8& pa3) {
;   for (int r = 0; r < 16; ++r) p1[r] = __builtin_amdgcn_exp2f(p1[r]);
;   float ps = 0; for (int r = 0; r < 16; ++r) ps += p0[r]; for (int r = 0; r < 16; ++r) ps += p1[r];
;   { auto rr = __builtin_amdgcn_permlane32_swap(__float_as_uint(ps), __float_as_uint(ps), false, false);
;     ps = __uint_as_float(rr[0]) + __uint_as_float(rr[1]); }
;   l_reg = l_reg * alpha + ps;
; template <bool HALF> __device__ __forceinline__ void dense_body(const bf16_t* __restrict__ Qb, const bf16_t* __restrict__ Kh, const bf16_t* __restrict__ Vh, ...
;     ...
;     RESC(alB); __syncthreads();
;     SBAR(); qkt<HALF>(pA0, pA1, Kl0, qr, r32, hi, koff);
;     finishSM(pB0, pB1, alB, l_reg, pa0, pa1, pa2, pa3); SBAR();
;     if (j + 3 < NT) SLOAD(SE, (j + 3) * KVBLK); SBAR();
;     pv_d0(o, vb0 + (int)SHM_V, pa0, pa1, pa2, pa3); partialSM(pA0, pA1, m_reg, mnA, alA);
;     __syncthreads(); SWAIT(); SWRITE(1, SO);
;     RESC(alA); __syncthreads();
;   }
.LBB0_435:
	v_cndmask_b32_e64 v170, v163, v230, s[42:43]
	v_mul_f32_e32 v146, 0xbe0293ee, v170
	v_mov_b32_e32 v147, v146
	v_fmamk_f32 v80, v80, 0x3e0293ee, v146
	v_fmamk_f32 v81, v81, 0x3e0293ee, v146
	v_fmamk_f32 v82, v82, 0x3e0293ee, v146
	v_fmamk_f32 v83, v83, 0x3e0293ee, v146
	v_fmamk_f32 v84, v84, 0x3e0293ee, v146
	v_fmamk_f32 v85, v85, 0x3e0293ee, v146
	v_fmamk_f32 v86, v86, 0x3e0293ee, v146
	v_fmamk_f32 v87, v87, 0x3e0293ee, v146
	v_fmamk_f32 v88, v88, 0x3e0293ee, v146
	v_fmamk_f32 v89, v89, 0x3e0293ee, v146
	v_fmamk_f32 v90, v90, 0x3e0293ee, v146
	v_fmamk_f32 v91, v91, 0x3e0293ee, v146
	v_fmamk_f32 v92, v92, 0x3e0293ee, v146
	v_fmamk_f32 v93, v93, 0x3e0293ee, v146
	v_fmamk_f32 v94, v94, 0x3e0293ee, v146
	v_fmac_f32_e32 v147, 0x3e0293ee, v95
	v_exp_f32_e32 v163, v80
	v_exp_f32_e32 v177, v81
	v_exp_f32_e32 v164, v82
	v_exp_f32_e32 v188, v83
	v_exp_f32_e32 v176, v84
	v_exp_f32_e32 v189, v85
	v_exp_f32_e32 v165, v86
	v_exp_f32_e32 v175, v87
	v_exp_f32_e32 v166, v88
	v_exp_f32_e32 v173, v89
	v_exp_f32_e32 v167, v90
	v_exp_f32_e32 v174, v91
	v_exp_f32_e32 v168, v92
	v_exp_f32_e32 v171, v93
	v_exp_f32_e32 v169, v94
	v_exp_f32_e32 v172, v147
	v_pk_fma_f32 v[160:161], v[64:65], s[10:11], v[146:147] op_sel_hi:[1,0,0]
	v_add_f32_e32 v64, v227, v228
	v_fmac_f32_e32 v64, v226, v202
	v_add_f32_e32 v202, v231, v232
	v_pk_fma_f32 v[158:159], v[66:67], s[10:11], v[146:147] op_sel_hi:[1,0,0]
	v_pk_fma_f32 v[154:155], v[68:69], s[10:11], v[146:147] op_sel_hi:[1,0,0]
	v_pk_fma_f32 v[150:151], v[70:71], s[10:11], v[146:147] op_sel_hi:[1,0,0]
	v_pk_fma_f32 v[148:149], v[72:73], s[10:11], v[146:147] op_sel_hi:[1,0,0]
	v_pk_fma_f32 v[156:157], v[74:75], s[10:11], v[146:147] op_sel_hi:[1,0,0]
	v_pk_fma_f32 v[152:153], v[76:77], s[10:11], v[146:147] op_sel_hi:[1,0,0]
	v_pk_fma_f32 v[146:147], v[78:79], s[10:11], v[146:147] op_sel_hi:[1,0,0]
	v_fmac_f32_e32 v202, v64, v229
	s_add_i32 s2, s2, 2
	s_and_b64 vcc, exec, s[20:21]
	s_waitcnt lgkmcnt(0)
	s_cbranch_vccnz .LBB0_437
	v_mov_b32_e32 v226, v162
	s_branch .LBB0_425

; #define SBAR() __builtin_amdgcn_sched_barrier(0)
; __device__ __forceinline__ void finishSM(f32x16& p0, f32x16& p1, float alpha, float& l_reg, bf16x8& pa0, bf16x8& pa1, bf16x8& pa2, bf16x8& pa3) {
;   for (int r = 0; r < 16; ++r) p1[r] = __builtin_amdgcn_exp2f(p1[r]);
;   float ps = 0; for (int r = 0; r < 16; ++r) ps += p0[r]; for (int r = 0; r < 16; ++r) ps += p1[r];
;   { auto rr = __builtin_amdgcn_permlane32_swap(__float_as_uint(ps), __float_as_uint(ps), false, false);
;     ps = __uint_as_float(rr[0]) + __uint_as_float(rr[1]); }
;   l_reg = l_reg * alpha + ps;
;     ...
;   PK4(p0, 0, pa0); PK4(p0, 8, pa1); PK4(p1, 0, pa2); PK4(p1, 8, pa3);
;     ...
; }
; template <bool HALF> __device__ __forceinline__ void qkt(f32x16& p0, f32x16& p1, const char* Ks, const bf16x8* qr, int r32, int hi, int koff) {
;   p0 = f32x16{}; p1 = f32x16{};
;   for (int d0 = 0; d0 < (HALF ? 4 : 8); ++d0) { int cb = (d0 * 16 + hi * 8) * 2 + koff;
;     bf16x8 b0 = *reinterpret_cast<const bf16x8*>(Ks + KSWZ(r32, cb));
;     bf16x8 b1 = *reinterpret_cast<const bf16x8*>(Ks + KSWZ(32 + r32, cb));
;     p0 = __builtin_amdgcn_mfma_f32_32x32x16_bf16(b0, qr[d0], p0, 0, 0, 0);
;     p1 = __builtin_amdgcn_mfma_f32_32x32x16_bf16(b1, qr[d0], p1, 0, 0, 0); }
; template <int D0> __device__ __forceinline__ void pv_one(f32x16& od, int vb, bf16x8 pa0, bf16x8 pa1, bf16x8 pa2, bf16x8 pa3) {
;   const s16x4 l0 = tr_read<v_rd_off(D0, 0, 0)>(vb), h0 = tr_read<v_rd_off(D0, 0, 1)>(vb), l1 = tr_read<v_rd_off(D0, 1, 0)>(vb), h1 = tr_read<v_rd_off(D0, 1, 1)>(vb);
;   const s16x4 l2 = tr_read<v_rd_off(D0, 2, 0)>(vb), h2 = tr_read<v_rd_off(D0, 2, 1)>(vb), l3 = tr_read<v_rd_off(D0, 3, 0)>(vb), h3 = tr_read<v_rd_off(D0, 3, 1)>(vb);
;   asm volatile("s_waitcnt lgkmcnt(0)" ::: "memory"); SBAR();
;     ...
;   od = __builtin_amdgcn_mfma_f32_32x32x16_bf16(pa0, PK(l0, h0), od, 0, 0, 0);
;   od = __builtin_amdgcn_mfma_f32_32x32x16_bf16(pa1, PK(l1, h1), od, 0, 0, 0);
;   od = __builtin_amdgcn_mfma_f32_32x32x16_bf16(pa2, PK(l2, h2), od, 0, 0, 0);
;   od = __builtin_amdgcn_mfma_f32_32x32x16_bf16(pa3, PK(l3, h3), od, 0, 0, 0);
;     ...
; }
; __device__ __forceinline__ void pv_d0(f32x16* o, int vb, bf16x8 pa0, bf16x8 pa1, bf16x8 pa2, bf16x8 pa3) {
;   pv_one<0>(o[0], vb, pa0, pa1, pa2, pa3); pv_one<1>(o[1], vb, pa0, pa1, pa2, pa3); pv_one<2>(o[2], vb, pa0, pa1, pa2, pa3); pv_one<3>(o[3], vb, pa0, pa1, pa2, pa3);
.LBB0_454:
	ds_read_b128 v[64:67], v192 offset:49152
	ds_read_b128 v[68:71], v192 offset:57344
	v_add_f32_e32 v146, 0, v147
	v_add_f32_e32 v146, v160, v146
	v_add_f32_e32 v146, v148, v146
	s_waitcnt lgkmcnt(1)
	v_mfma_f32_32x32x16_bf16 v[80:95], v[64:67], v[98:101], 0
	v_add_f32_e32 v146, v161, v146
	v_add_f32_e32 v146, v149, v146
	ds_read_b128 v[172:175], v193 offset:49152
	ds_read_b128 v[198:201], v193 offset:57344
	v_add_f32_e32 v146, v170, v146
	v_add_f32_e32 v146, v159, v146
	v_add_f32_e32 v146, v171, v146
	v_add_f32_e32 v146, v151, v146
	s_waitcnt lgkmcnt(2)
	v_mfma_f32_32x32x16_bf16 v[64:79], v[68:71], v[98:101], 0
	v_add_f32_e32 v146, v155, v146
	v_add_f32_e32 v146, v152, v146
	v_add_f32_e32 v146, v156, v146
	v_exp_f32_e32 v144, v144
	v_add_f32_e32 v146, v153, v146
	v_exp_f32_e32 v145, v145
	v_add_f32_e32 v146, v157, v146
	s_waitcnt lgkmcnt(1)
	v_mfma_f32_32x32x16_bf16 v[80:95], v[172:175], v[106:109], v[80:95]
	v_exp_f32_e32 v142, v142
	v_add_f32_e32 v146, v154, v146
	v_exp_f32_e32 v143, v143
	v_add_f32_e32 v146, v158, v146
	v_exp_f32_e32 v138, v138
	v_add_f32_e32 v146, v144, v146
	v_exp_f32_e32 v139, v139
	s_waitcnt lgkmcnt(0)
	v_mfma_f32_32x32x16_bf16 v[64:79], v[198:201], v[106:109], v[64:79]
	ds_read_b128 v[172:175], v195 offset:49152
	ds_read_b128 v[198:201], v195 offset:57344
	v_add_f32_e32 v146, v145, v146
	v_exp_f32_e32 v134, v134
	v_add_f32_e32 v146, v142, v146
	v_exp_f32_e32 v135, v135
	v_add_f32_e32 v146, v143, v146
	v_exp_f32_e32 v132, v132
	s_waitcnt lgkmcnt(1)
	v_mfma_f32_32x32x16_bf16 v[80:95], v[172:175], v[110:113], v[80:95]
	v_add_f32_e32 v146, v138, v146
	v_exp_f32_e32 v133, v133
	v_add_f32_e32 v146, v139, v146
	v_exp_f32_e32 v140, v140
	v_add_f32_e32 v146, v134, v146
	v_exp_f32_e32 v141, v141
	v_add_f32_e32 v146, v135, v146
	s_waitcnt lgkmcnt(0)
	v_mfma_f32_32x32x16_bf16 v[64:79], v[198:201], v[110:113], v[64:79]
	ds_read_b128 v[172:175], v194 offset:49152
	ds_read_b128 v[198:201], v194 offset:57344
	v_exp_f32_e32 v136, v136
	v_add_f32_e32 v146, v132, v146
	v_exp_f32_e32 v137, v137
	v_add_f32_e32 v146, v133, v146
	v_exp_f32_e32 v130, v130
	v_add_f32_e32 v146, v140, v146
	s_waitcnt lgkmcnt(1)
	v_mfma_f32_32x32x16_bf16 v[80:95], v[172:175], v[102:105], v[80:95]
	v_exp_f32_e32 v131, v131
	v_add_f32_e32 v146, v141, v146
	v_add_f32_e32 v146, v136, v146
	v_add_f32_e32 v146, v137, v146
	v_add_f32_e32 v146, v130, v146
	s_waitcnt lgkmcnt(0)
	v_mfma_f32_32x32x16_bf16 v[64:79], v[198:201], v[102:105], v[64:79]
	v_add_f32_e32 v198, v131, v146
	v_mov_b32_e32 v199, v198
	v_cvt_pk_bf16_f32 v146, v147, v160
	v_cvt_pk_bf16_f32 v147, v148, v161
	v_cvt_pk_bf16_f32 v148, v149, v170
	v_cvt_pk_bf16_f32 v149, v159, v171
	v_cvt_pk_bf16_f32 v200, v151, v155
	v_cvt_pk_bf16_f32 v201, v152, v156
	v_cvt_pk_bf16_f32 v202, v153, v157
	s_nop 1
	v_permlane32_swap_b32_e32 v198, v199
	v_permlane32_swap_b32_e32 v146, v148
	v_cvt_pk_bf16_f32 v203, v154, v158
	v_permlane32_swap_b32_e32 v200, v202
	v_cvt_pk_bf16_f32 v152, v144, v145
	v_cvt_pk_bf16_f32 v153, v142, v143
	v_cvt_pk_bf16_f32 v154, v138, v139
	v_cvt_pk_bf16_f32 v155, v134, v135
	v_cvt_pk_bf16_f32 v156, v132, v133
	v_cvt_pk_bf16_f32 v157, v140, v141
	v_cvt_pk_bf16_f32 v158, v136, v137
	v_cvt_pk_bf16_f32 v159, v130, v131
	v_permlane32_swap_b32_e32 v147, v149
	v_permlane32_swap_b32_e32 v201, v203
	v_permlane32_swap_b32_e32 v152, v154
	v_permlane32_swap_b32_e32 v153, v155
	v_permlane32_swap_b32_e32 v156, v158
	v_permlane32_swap_b32_e32 v157, v159
	ds_read_b64_tr_b16 v[204:205], v187 offset:0
	ds_read_b64_tr_b16 v[206:207], v187 offset:0x800
	ds_read_b64_tr_b16 v[208:209], v187 offset:0x1000
	ds_read_b64_tr_b16 v[210:211], v187 offset:0x1800
	ds_read_b64_tr_b16 v[212:213], v187 offset:0x2000
	ds_read_b64_tr_b16 v[214:215], v187 offset:0x2800
	ds_read_b64_tr_b16 v[222:223], v187 offset:0x3000
	ds_read_b64_tr_b16 v[224:225], v187 offset:0x3800
	s_waitcnt lgkmcnt(0)
	s_nop 0
	v_mfma_f32_32x32x16_bf16 v[0:15], v[146:149], v[204:207], v[0:15]
	ds_read_b64_tr_b16 v[204:205], v187 offset:0x200
	ds_read_b64_tr_b16 v[206:207], v187 offset:0xa00
	v_mfma_f32_32x32x16_bf16 v[0:15], v[200:203], v[208:211], v[0:15]
	ds_read_b64_tr_b16 v[208:209], v187 offset:0x1200
	ds_read_b64_tr_b16 v[210:211], v187 offset:0x1a00
	v_mfma_f32_32x32x16_bf16 v[0:15], v[152:155], v[212:215], v[0:15]
	ds_read_b64_tr_b16 v[212:213], v187 offset:0x2200
	ds_read_b64_tr_b16 v[214:215], v187 offset:0x2a00
	v_mfma_f32_32x32x16_bf16 v[0:15], v[156:159], v[222:225], v[0:15]
	ds_read_b64_tr_b16 v[222:223], v187 offset:0x3200
	ds_read_b64_tr_b16 v[224:225], v187 offset:0x3a00
	s_waitcnt lgkmcnt(0)
	v_mfma_f32_32x32x16_bf16 v[48:63], v[146:149], v[204:207], v[48:63]
	ds_read_b64_tr_b16 v[204:205], v187 offset:0x400
	ds_read_b64_tr_b16 v[206:207], v187 offset:0xc00
	v_mfma_f32_32x32x16_bf16 v[48:63], v[200:203], v[208:211], v[48:63]
	ds_read_b64_tr_b16 v[208:209], v187 offset:0x1400
	ds_read_b64_tr_b16 v[210:211], v187 offset:0x1c00
	v_mfma_f32_32x32x16_bf16 v[48:63], v[152:155], v[212:215], v[48:63]
	ds_read_b64_tr_b16 v[212:213], v187 offset:0x2400
	ds_read_b64_tr_b16 v[214:215], v187 offset:0x2c00
	v_mfma_f32_32x32x16_bf16 v[48:63], v[156:159], v[222:225], v[48:63]
	ds_read_b64_tr_b16 v[222:223], v187 offset:0x3400
	ds_read_b64_tr_b16 v[224:225], v187 offset:0x3c00
	s_waitcnt lgkmcnt(0)
; #define SBAR() __builtin_amdgcn_sched_barrier(0)
; __device__ __forceinline__ void partialSM(f32x16& p0, f32x16& p1, float& m_reg, float& mn, float& alpha) {
;     ...
;   float pmax = p0[0]; for (int r = 1; r < 16; ++r) pmax = fmaxf(pmax, p0[r]); for (int r = 0; r < 16; ++r) pmax = fmaxf(pmax, p1[r]);
;   { auto rr = __builtin_amdgcn_permlane32_swap(__float_as_uint(pmax), __float_as_uint(pmax), false, false);
;     pmax = fmaxf(__uint_as_float(rr[0]), __uint_as_float(rr[1])); }
;   if (__builtin_expect(__all(pmax - m_reg <= THR / SCALE), 1)) { mn = m_reg; alpha = 1.f; }
;   else { mn = fmaxf(m_reg, pmax); alpha = __builtin_amdgcn_exp2f((m_reg - mn) * C); m_reg = mn; }
; template <int D0> __device__ __forceinline__ void pv_one(f32x16& od, int vb, bf16x8 pa0, bf16x8 pa1, bf16x8 pa2, bf16x8 pa3) {
;   const s16x4 l0 = tr_read<v_rd_off(D0, 0, 0)>(vb), h0 = tr_read<v_rd_off(D0, 0, 1)>(vb), l1 = tr_read<v_rd_off(D0, 1, 0)>(vb), h1 = tr_read<v_rd_off(D0, 1, 1)>(vb);
;   const s16x4 l2 = tr_read<v_rd_off(D0, 2, 0)>(vb), h2 = tr_read<v_rd_off(D0, 2, 1)>(vb), l3 = tr_read<v_rd_off(D0, 3, 0)>(vb), h3 = tr_read<v_rd_off(D0, 3, 1)>(vb);
;   asm volatile("s_waitcnt lgkmcnt(0)" ::: "memory"); SBAR();
;     ...
;   od = __builtin_amdgcn_mfma_f32_32x32x16_bf16(pa0, PK(l0, h0), od, 0, 0, 0);
;   od = __builtin_amdgcn_mfma_f32_32x32x16_bf16(pa1, PK(l1, h1), od, 0, 0, 0);
;   od = __builtin_amdgcn_mfma_f32_32x32x16_bf16(pa2, PK(l2, h2), od, 0, 0, 0);
;   od = __builtin_amdgcn_mfma_f32_32x32x16_bf16(pa3, PK(l3, h3), od, 0, 0, 0);
;     ...
; }
; __device__ __forceinline__ void pv_d0(f32x16* o, int vb, bf16x8 pa0, bf16x8 pa1, bf16x8 pa2, bf16x8 pa3) {
;   pv_one<0>(o[0], vb, pa0, pa1, pa2, pa3); pv_one<1>(o[1], vb, pa0, pa1, pa2, pa3); pv_one<2>(o[2], vb, pa0, pa1, pa2, pa3); pv_one<3>(o[3], vb, pa0, pa1, pa2, pa3);
	v_mfma_f32_32x32x16_bf16 v[32:47], v[146:149], v[204:207], v[32:47]
	ds_read_b64_tr_b16 v[204:205], v187 offset:0x600
	ds_read_b64_tr_b16 v[206:207], v187 offset:0xe00
	v_mfma_f32_32x32x16_bf16 v[32:47], v[200:203], v[208:211], v[32:47]
	ds_read_b64_tr_b16 v[208:209], v187 offset:0x1600
	ds_read_b64_tr_b16 v[210:211], v187 offset:0x1e00
	v_mfma_f32_32x32x16_bf16 v[32:47], v[152:155], v[212:215], v[32:47]
	ds_read_b64_tr_b16 v[212:213], v187 offset:0x2600
	ds_read_b64_tr_b16 v[214:215], v187 offset:0x2e00
	v_mfma_f32_32x32x16_bf16 v[32:47], v[156:159], v[222:225], v[32:47]
	ds_read_b64_tr_b16 v[222:223], v187 offset:0x3600
	ds_read_b64_tr_b16 v[224:225], v187 offset:0x3e00
	s_waitcnt lgkmcnt(0)
	v_mfma_f32_32x32x16_bf16 v[16:31], v[146:149], v[204:207], v[16:31]
	v_max_f32_e32 v146, v81, v81
	v_max_f32_e32 v147, v80, v80
	v_max_f32_e32 v146, v147, v146
	v_max3_f32 v146, v146, v82, v83
	v_max3_f32 v146, v146, v84, v85
	v_max3_f32 v146, v146, v86, v87
	v_max3_f32 v146, v146, v88, v89
	v_max3_f32 v146, v146, v90, v91
	v_max3_f32 v146, v146, v92, v93
	v_mfma_f32_32x32x16_bf16 v[16:31], v[200:203], v[208:211], v[16:31]
	v_max3_f32 v146, v146, v94, v95
	v_max3_f32 v146, v146, v64, v65
	v_max3_f32 v146, v146, v66, v67
	v_max3_f32 v146, v146, v68, v69
	v_max3_f32 v146, v146, v70, v71
	v_max3_f32 v146, v146, v72, v73
	v_max3_f32 v146, v146, v74, v75
	v_max3_f32 v146, v146, v76, v77
	v_mfma_f32_32x32x16_bf16 v[16:31], v[152:155], v[212:215], v[16:31]
	v_max3_f32 v146, v146, v78, v79
	v_mov_b32_e32 v147, v146
	s_nop 1
	v_permlane32_swap_b32_e32 v146, v147
	v_max_f32_e32 v147, v147, v147
	v_max_f32_e32 v146, v146, v146
	v_max_f32_e32 v146, v146, v147
	v_sub_f32_e32 v147, v146, v150
	v_cmp_ge_f32_e32 vcc, s87, v147
	v_max_f32_e32 v147, v150, v150
	v_max_f32_e32 v146, v147, v146
	v_mfma_f32_32x32x16_bf16 v[16:31], v[156:159], v[222:225], v[16:31]
	v_sub_f32_e32 v147, v150, v146
	v_mul_f32_e32 v147, 0x3e0293ee, v147
	v_exp_f32_e32 v147, v147
	s_cmp_eq_u64 vcc, exec
	s_cselect_b64 s[42:43], -1, 0
	s_waitcnt vmcnt(0)
	s_barrier
	s_add_i32 m0, s52, 0x4000
	s_nop 0
	global_load_lds_dwordx4 v232, s[48:49]
	s_add_i32 m0, s52, 0x4400
	s_nop 0
	global_load_lds_dwordx4 v233, s[48:49]
	s_add_i32 m0, s53, 0x0
	s_nop 0
	global_load_lds_dwordx4 v234, s[50:51]
	s_add_i32 m0, s53, 0x400
	s_nop 0
	global_load_lds_dwordx4 v235, s[50:51]
	s_add_u32 s48, s48, 0x18000
	s_addc_u32 s49, s49, 0
	s_add_u32 s50, s50, 0xc0000
	s_addc_u32 s51, s51, 0
	v_cndmask_b32_e64 v200, v147, 1.0, s[42:43]
	v_cmp_gt_f32_e32 vcc, 1.0, v200
	s_cbranch_vccz .LBB0_458
	s_and_saveexec_b64 s[6:7], s[40:41]
	ds_write_b32 v184, v200 offset:128
	s_or_b64 exec, exec, s[6:7]
	s_waitcnt lgkmcnt(0)
	v_add_u32_e32 v147, v183, v96
	ds_read_b128 v[152:155], v147 offset:224
	ds_read_b128 v[156:159], v147 offset:192
	ds_read_b128 v[202:205], v147 offset:160
	ds_read_b128 v[206:209], v147 offset:128
	s_waitcnt lgkmcnt(3)
	v_pk_mul_f32 v[12:13], v[12:13], v[152:153]
	s_waitcnt lgkmcnt(2)
	v_pk_mul_f32 v[8:9], v[8:9], v[156:157]
	s_waitcnt lgkmcnt(1)
	v_pk_mul_f32 v[4:5], v[4:5], v[202:203]
	v_pk_mul_f32 v[14:15], v[14:15], v[154:155]
	v_pk_mul_f32 v[10:11], v[10:11], v[158:159]
	v_pk_mul_f32 v[6:7], v[6:7], v[204:205]
	s_waitcnt lgkmcnt(0)
	v_pk_mul_f32 v[2:3], v[2:3], v[208:209]
	v_pk_mul_f32 v[0:1], v[0:1], v[206:207]
	v_pk_mul_f32 v[60:61], v[60:61], v[152:153]
	v_pk_mul_f32 v[56:57], v[56:57], v[156:157]
	v_pk_mul_f32 v[52:53], v[52:53], v[202:203]
	v_pk_mul_f32 v[62:63], v[62:63], v[154:155]
	v_pk_mul_f32 v[58:59], v[58:59], v[158:159]
	v_pk_mul_f32 v[54:55], v[54:55], v[204:205]
	v_pk_mul_f32 v[50:51], v[50:51], v[208:209]
	v_pk_mul_f32 v[48:49], v[48:49], v[206:207]
	v_pk_mul_f32 v[44:45], v[44:45], v[152:153]
	v_pk_mul_f32 v[40:41], v[40:41], v[156:157]
	v_pk_mul_f32 v[36:37], v[36:37], v[202:203]
	v_pk_mul_f32 v[46:47], v[46:47], v[154:155]
	v_pk_mul_f32 v[42:43], v[42:43], v[158:159]
	v_pk_mul_f32 v[38:39], v[38:39], v[204:205]
	v_pk_mul_f32 v[34:35], v[34:35], v[208:209]
	v_pk_mul_f32 v[32:33], v[32:33], v[206:207]
	v_pk_mul_f32 v[28:29], v[28:29], v[152:153]
	v_pk_mul_f32 v[24:25], v[24:25], v[156:157]
	v_pk_mul_f32 v[20:21], v[20:21], v[202:203]
	v_pk_mul_f32 v[30:31], v[30:31], v[154:155]
	v_pk_mul_f32 v[26:27], v[26:27], v[158:159]
	v_pk_mul_f32 v[22:23], v[22:23], v[204:205]
	v_pk_mul_f32 v[18:19], v[18:19], v[208:209]
	v_pk_mul_f32 v[16:17], v[16:17], v[206:207]
; __device__ __forceinline__ void partialSM(f32x16& p0, f32x16& p1, float& m_reg, float& mn, float& alpha) {
;     ...
;   float mnC = -mn * C;
;   for (int r = 0; r < 16; ++r) p0[r] = fmaf(p0[r], C, mnC); for (int r = 0; r < 16; ++r) p1[r] = fmaf(p1[r], C, mnC);
;   for (int r = 0; r < 16; ++r) p0[r] = __builtin_amdgcn_exp2f(p0[r]);
; __device__ __forceinline__ void finishSM(f32x16& p0, f32x16& p1, float alpha, float& l_reg, bf16x8& pa0, bf16x8& pa1, bf16x8& pa2, bf16x8& pa3) {
;   for (int r = 0; r < 16; ++r) p1[r] = __builtin_amdgcn_exp2f(p1[r]);
;   float ps = 0; for (int r = 0; r < 16; ++r) ps += p0[r]; for (int r = 0; r < 16; ++r) ps += p1[r];
;   { auto rr = __builtin_amdgcn_permlane32_swap(__float_as_uint(ps), __float_as_uint(ps), false, false);
;     ps = __uint_as_float(rr[0]) + __uint_as_float(rr[1]); }
;   l_reg = l_reg * alpha + ps;
;     ...
;   PK4(p0, 0, pa0); PK4(p0, 8, pa1); PK4(p1, 0, pa2); PK4(p1, 8, pa3);
;     ...
; }
; template <bool HALF> __device__ __forceinline__ void qkt(f32x16& p0, f32x16& p1, const char* Ks, const bf16x8* qr, int r32, int hi, int koff) {
;   p0 = f32x16{}; p1 = f32x16{};
;   for (int d0 = 0; d0 < (HALF ? 4 : 8); ++d0) { int cb = (d0 * 16 + hi * 8) * 2 + koff;
;     bf16x8 b0 = *reinterpret_cast<const bf16x8*>(Ks + KSWZ(r32, cb));
;     bf16x8 b1 = *reinterpret_cast<const bf16x8*>(Ks + KSWZ(32 + r32, cb));
;     p0 = __builtin_amdgcn_mfma_f32_32x32x16_bf16(b0, qr[d0], p0, 0, 0, 0);
;     p1 = __builtin_amdgcn_mfma_f32_32x32x16_bf16(b1, qr[d0], p1, 0, 0, 0); }
.LBB0_458:
	v_cndmask_b32_e64 v201, v146, v150, s[42:43]
	v_mul_f32_e32 v202, 0xbe0293ee, v201
	v_fmamk_f32 v80, v80, 0x3e0293ee, v202
	v_fmamk_f32 v81, v81, 0x3e0293ee, v202
	v_fmamk_f32 v82, v82, 0x3e0293ee, v202
	v_fmamk_f32 v83, v83, 0x3e0293ee, v202
	v_fmamk_f32 v84, v84, 0x3e0293ee, v202
	v_fmamk_f32 v85, v85, 0x3e0293ee, v202
	v_fmamk_f32 v86, v86, 0x3e0293ee, v202
	v_fmamk_f32 v87, v87, 0x3e0293ee, v202
	v_fmamk_f32 v88, v88, 0x3e0293ee, v202
	v_fmamk_f32 v89, v89, 0x3e0293ee, v202
	v_fmamk_f32 v90, v90, 0x3e0293ee, v202
	v_fmamk_f32 v91, v91, 0x3e0293ee, v202
	v_fmamk_f32 v92, v92, 0x3e0293ee, v202
	v_fmamk_f32 v93, v93, 0x3e0293ee, v202
	v_fmamk_f32 v94, v94, 0x3e0293ee, v202
	v_fmamk_f32 v95, v95, 0x3e0293ee, v202
	v_exp_f32_e32 v146, v80
	v_exp_f32_e32 v161, v81
	v_exp_f32_e32 v147, v82
	v_exp_f32_e32 v160, v83
	v_exp_f32_e32 v148, v84
	v_exp_f32_e32 v159, v85
	v_exp_f32_e32 v149, v86
	v_exp_f32_e32 v158, v87
	v_exp_f32_e32 v150, v88
	v_exp_f32_e32 v157, v89
	v_exp_f32_e32 v151, v90
	v_exp_f32_e32 v156, v91
	v_exp_f32_e32 v152, v92
	v_exp_f32_e32 v155, v93
	v_exp_f32_e32 v153, v94
	v_exp_f32_e32 v154, v95
	v_fmamk_f32 v211, v64, 0x3e0293ee, v202
	v_fmamk_f32 v221, v65, 0x3e0293ee, v202
	v_fmamk_f32 v222, v66, 0x3e0293ee, v202
	v_fmamk_f32 v223, v67, 0x3e0293ee, v202
	v_fmamk_f32 v224, v68, 0x3e0293ee, v202
	v_fmamk_f32 v204, v69, 0x3e0293ee, v202
	v_fmamk_f32 v205, v70, 0x3e0293ee, v202
	v_fmamk_f32 v206, v71, 0x3e0293ee, v202
	v_fmamk_f32 v207, v72, 0x3e0293ee, v202
	v_fmamk_f32 v208, v73, 0x3e0293ee, v202
	v_fmamk_f32 v209, v74, 0x3e0293ee, v202
	v_fmamk_f32 v210, v75, 0x3e0293ee, v202
	v_fmamk_f32 v203, v76, 0x3e0293ee, v202
	v_fmamk_f32 v225, v77, 0x3e0293ee, v202
	v_fmamk_f32 v226, v78, 0x3e0293ee, v202
	v_fmac_f32_e32 v202, 0x3e0293ee, v79
	s_waitcnt lgkmcnt(0)
	ds_read_b128 v[64:67], v192 offset:32768
	ds_read_b128 v[68:71], v192 offset:40960
	ds_read_b128 v[212:215], v193 offset:32768
	ds_read_b128 v[228:231], v193 offset:40960
	v_exp_f32_e32 v211, v211
	v_exp_f32_e32 v204, v204
	s_waitcnt lgkmcnt(3)
	v_mfma_f32_32x32x16_bf16 v[80:95], v[64:67], v[98:101], 0
	v_exp_f32_e32 v205, v205
	v_exp_f32_e32 v206, v206
	v_exp_f32_e32 v207, v207
	v_exp_f32_e32 v208, v208
	v_exp_f32_e32 v209, v209
	v_exp_f32_e32 v210, v210
	s_waitcnt lgkmcnt(2)
	v_mfma_f32_32x32x16_bf16 v[64:79], v[68:71], v[98:101], 0
	s_waitcnt lgkmcnt(1)
	v_mfma_f32_32x32x16_bf16 v[80:95], v[212:215], v[106:109], v[80:95]
	s_waitcnt lgkmcnt(0)
	v_mfma_f32_32x32x16_bf16 v[64:79], v[228:231], v[106:109], v[64:79]
	ds_read_b128 v[212:215], v195 offset:32768
	ds_read_b128 v[228:231], v195 offset:40960
	s_waitcnt lgkmcnt(1)
	v_mfma_f32_32x32x16_bf16 v[80:95], v[212:215], v[110:113], v[80:95]
	s_waitcnt lgkmcnt(0)
	v_mfma_f32_32x32x16_bf16 v[64:79], v[228:231], v[110:113], v[64:79]
	ds_read_b128 v[212:215], v194 offset:32768
	ds_read_b128 v[228:231], v194 offset:40960
	s_waitcnt lgkmcnt(1)
	v_mfma_f32_32x32x16_bf16 v[80:95], v[212:215], v[102:105], v[80:95]
	v_exp_f32_e32 v215, v224
	v_exp_f32_e32 v224, v202
	v_add_f32_e32 v202, 0, v146
	v_add_f32_e32 v202, v161, v202
	v_add_f32_e32 v202, v147, v202
	v_add_f32_e32 v202, v160, v202
	v_add_f32_e32 v202, v148, v202
	v_add_f32_e32 v202, v159, v202
	v_add_f32_e32 v202, v149, v202
	v_add_f32_e32 v202, v158, v202
	v_add_f32_e32 v202, v150, v202
	v_add_f32_e32 v202, v157, v202
	v_add_f32_e32 v202, v151, v202
	v_add_f32_e32 v202, v156, v202
	v_add_f32_e32 v202, v152, v202
	v_exp_f32_e32 v212, v221
	v_add_f32_e32 v202, v155, v202
	v_exp_f32_e32 v213, v222
	v_add_f32_e32 v202, v153, v202
	v_exp_f32_e32 v214, v223
	v_add_f32_e32 v202, v154, v202
	v_add_f32_e32 v202, v211, v202
	v_add_f32_e32 v202, v212, v202
	v_add_f32_e32 v202, v213, v202
	v_add_f32_e32 v202, v214, v202
	v_add_f32_e32 v202, v215, v202
	v_add_f32_e32 v202, v204, v202
	v_add_f32_e32 v202, v205, v202
	v_add_f32_e32 v202, v206, v202
	v_exp_f32_e32 v221, v203
	v_add_f32_e32 v202, v207, v202
	v_exp_f32_e32 v222, v225
	v_add_f32_e32 v202, v208, v202
	s_waitcnt lgkmcnt(0)
	v_mfma_f32_32x32x16_bf16 v[64:79], v[228:231], v[102:105], v[64:79]
	v_exp_f32_e32 v223, v226
	v_add_f32_e32 v202, v209, v202
	v_add_f32_e32 v202, v210, v202
	v_add_f32_e32 v202, v221, v202
	v_add_f32_e32 v202, v222, v202
	v_add_f32_e32 v202, v223, v202
	v_add_f32_e32 v202, v224, v202
	v_mov_b32_e32 v203, v202
	v_cvt_pk_bf16_f32 v146, v146, v161
	v_cvt_pk_bf16_f32 v147, v147, v160
	v_cvt_pk_bf16_f32 v148, v148, v159
	v_cvt_pk_bf16_f32 v149, v149, v158
	v_cvt_pk_bf16_f32 v150, v150, v157
	v_cvt_pk_bf16_f32 v151, v151, v156
	v_cvt_pk_bf16_f32 v152, v152, v155
	v_cvt_pk_bf16_f32 v153, v153, v154
	v_cvt_pk_bf16_f32 v154, v211, v212
	v_cvt_pk_bf16_f32 v155, v213, v214
	v_cvt_pk_bf16_f32 v156, v215, v204
	v_cvt_pk_bf16_f32 v157, v205, v206
	v_cvt_pk_bf16_f32 v158, v207, v208
	v_cvt_pk_bf16_f32 v159, v209, v210
	v_cvt_pk_bf16_f32 v160, v221, v222
	v_cvt_pk_bf16_f32 v161, v223, v224
	s_nop 1
	v_permlane32_swap_b32_e32 v202, v203
	v_permlane32_swap_b32_e32 v146, v148
	v_permlane32_swap_b32_e32 v147, v149
	v_permlane32_swap_b32_e32 v150, v152
	v_permlane32_swap_b32_e32 v151, v153
	v_permlane32_swap_b32_e32 v154, v156
	v_permlane32_swap_b32_e32 v155, v157
	v_permlane32_swap_b32_e32 v158, v160
	v_permlane32_swap_b32_e32 v159, v161
	s_cmp_ge_u32 s3, s24
	s_cselect_b64 s[14:15], -1, 0
; #define SBAR() __builtin_amdgcn_sched_barrier(0)
; __device__ __forceinline__ void partialSM(f32x16& p0, f32x16& p1, float& m_reg, float& mn, float& alpha) {
;     ...
;   float pmax = p0[0]; for (int r = 1; r < 16; ++r) pmax = fmaxf(pmax, p0[r]); for (int r = 0; r < 16; ++r) pmax = fmaxf(pmax, p1[r]);
;   { auto rr = __builtin_amdgcn_permlane32_swap(__float_as_uint(pmax), __float_as_uint(pmax), false, false);
;     pmax = fmaxf(__uint_as_float(rr[0]), __uint_as_float(rr[1])); }
;   if (__builtin_expect(__all(pmax - m_reg <= THR / SCALE), 1)) { mn = m_reg; alpha = 1.f; }
;   else { mn = fmaxf(m_reg, pmax); alpha = __builtin_amdgcn_exp2f((m_reg - mn) * C); m_reg = mn; }
; template <int D0> __device__ __forceinline__ void pv_one(f32x16& od, int vb, bf16x8 pa0, bf16x8 pa1, bf16x8 pa2, bf16x8 pa3) {
;   const s16x4 l0 = tr_read<v_rd_off(D0, 0, 0)>(vb), h0 = tr_read<v_rd_off(D0, 0, 1)>(vb), l1 = tr_read<v_rd_off(D0, 1, 0)>(vb), h1 = tr_read<v_rd_off(D0, 1, 1)>(vb);
;   const s16x4 l2 = tr_read<v_rd_off(D0, 2, 0)>(vb), h2 = tr_read<v_rd_off(D0, 2, 1)>(vb), l3 = tr_read<v_rd_off(D0, 3, 0)>(vb), h3 = tr_read<v_rd_off(D0, 3, 1)>(vb);
;   asm volatile("s_waitcnt lgkmcnt(0)" ::: "memory"); SBAR();
;     ...
;   od = __builtin_amdgcn_mfma_f32_32x32x16_bf16(pa0, PK(l0, h0), od, 0, 0, 0);
;   od = __builtin_amdgcn_mfma_f32_32x32x16_bf16(pa1, PK(l1, h1), od, 0, 0, 0);
;   od = __builtin_amdgcn_mfma_f32_32x32x16_bf16(pa2, PK(l2, h2), od, 0, 0, 0);
;   od = __builtin_amdgcn_mfma_f32_32x32x16_bf16(pa3, PK(l3, h3), od, 0, 0, 0);
;     ...
; }
; __device__ __forceinline__ void pv_d0(f32x16* o, int vb, bf16x8 pa0, bf16x8 pa1, bf16x8 pa2, bf16x8 pa3) {
;   pv_one<0>(o[0], vb, pa0, pa1, pa2, pa3); pv_one<1>(o[1], vb, pa0, pa1, pa2, pa3); pv_one<2>(o[2], vb, pa0, pa1, pa2, pa3); pv_one<3>(o[3], vb, pa0, pa1, pa2, pa3);
.LBB0_460:
	ds_read_b64_tr_b16 v[170:171], v186 offset:0
	ds_read_b64_tr_b16 v[172:173], v186 offset:0x800
	ds_read_b64_tr_b16 v[174:175], v186 offset:0x1000
	ds_read_b64_tr_b16 v[176:177], v186 offset:0x1800
	ds_read_b64_tr_b16 v[204:205], v186 offset:0x2000
	ds_read_b64_tr_b16 v[206:207], v186 offset:0x2800
	ds_read_b64_tr_b16 v[208:209], v186 offset:0x3000
	ds_read_b64_tr_b16 v[210:211], v186 offset:0x3800
	s_waitcnt lgkmcnt(0)
	s_nop 0
	v_mfma_f32_32x32x16_bf16 v[0:15], v[146:149], v[170:173], v[0:15]
	ds_read_b64_tr_b16 v[170:171], v186 offset:0x200
	ds_read_b64_tr_b16 v[172:173], v186 offset:0xa00
	v_mfma_f32_32x32x16_bf16 v[0:15], v[150:153], v[174:177], v[0:15]
	ds_read_b64_tr_b16 v[174:175], v186 offset:0x1200
	ds_read_b64_tr_b16 v[176:177], v186 offset:0x1a00
	v_mfma_f32_32x32x16_bf16 v[0:15], v[154:157], v[204:207], v[0:15]
	ds_read_b64_tr_b16 v[204:205], v186 offset:0x2200
	ds_read_b64_tr_b16 v[206:207], v186 offset:0x2a00
	v_mfma_f32_32x32x16_bf16 v[0:15], v[158:161], v[208:211], v[0:15]
	ds_read_b64_tr_b16 v[208:209], v186 offset:0x3200
	ds_read_b64_tr_b16 v[210:211], v186 offset:0x3a00
	s_waitcnt lgkmcnt(0)
	v_mfma_f32_32x32x16_bf16 v[48:63], v[146:149], v[170:173], v[48:63]
	ds_read_b64_tr_b16 v[170:171], v186 offset:0x400
	ds_read_b64_tr_b16 v[172:173], v186 offset:0xc00
	v_mfma_f32_32x32x16_bf16 v[48:63], v[150:153], v[174:177], v[48:63]
	ds_read_b64_tr_b16 v[174:175], v186 offset:0x1400
	ds_read_b64_tr_b16 v[176:177], v186 offset:0x1c00
	v_mfma_f32_32x32x16_bf16 v[48:63], v[154:157], v[204:207], v[48:63]
	ds_read_b64_tr_b16 v[204:205], v186 offset:0x2400
	ds_read_b64_tr_b16 v[206:207], v186 offset:0x2c00
	v_mfma_f32_32x32x16_bf16 v[48:63], v[158:161], v[208:211], v[48:63]
	ds_read_b64_tr_b16 v[208:209], v186 offset:0x3400
	ds_read_b64_tr_b16 v[210:211], v186 offset:0x3c00
	s_waitcnt lgkmcnt(0)
	v_mfma_f32_32x32x16_bf16 v[32:47], v[146:149], v[170:173], v[32:47]
	ds_read_b64_tr_b16 v[170:171], v186 offset:0x600
	ds_read_b64_tr_b16 v[172:173], v186 offset:0xe00
	v_mfma_f32_32x32x16_bf16 v[32:47], v[150:153], v[174:177], v[32:47]
	ds_read_b64_tr_b16 v[174:175], v186 offset:0x1600
	ds_read_b64_tr_b16 v[176:177], v186 offset:0x1e00
	v_mfma_f32_32x32x16_bf16 v[32:47], v[154:157], v[204:207], v[32:47]
	ds_read_b64_tr_b16 v[204:205], v186 offset:0x2600
	ds_read_b64_tr_b16 v[206:207], v186 offset:0x2e00
	v_mfma_f32_32x32x16_bf16 v[32:47], v[158:161], v[208:211], v[32:47]
	ds_read_b64_tr_b16 v[208:209], v186 offset:0x3600
	ds_read_b64_tr_b16 v[210:211], v186 offset:0x3e00
	s_waitcnt lgkmcnt(0)
	v_mfma_f32_32x32x16_bf16 v[16:31], v[146:149], v[170:173], v[16:31]
	v_max_f32_e32 v146, v81, v81
	v_max_f32_e32 v147, v80, v80
	v_max_f32_e32 v146, v147, v146
	v_max3_f32 v146, v146, v82, v83
	v_max3_f32 v146, v146, v84, v85
	v_max3_f32 v146, v146, v86, v87
	v_max3_f32 v146, v146, v88, v89
	v_max3_f32 v146, v146, v90, v91
	v_max3_f32 v146, v146, v92, v93
	v_mfma_f32_32x32x16_bf16 v[16:31], v[150:153], v[174:177], v[16:31]
	v_max3_f32 v146, v146, v94, v95
	v_max3_f32 v146, v146, v64, v65
	v_max3_f32 v146, v146, v66, v67
	v_max3_f32 v146, v146, v68, v69
	v_max3_f32 v146, v146, v70, v71
	v_max3_f32 v146, v146, v72, v73
	v_max3_f32 v146, v146, v74, v75
	v_max3_f32 v146, v146, v76, v77
	v_mfma_f32_32x32x16_bf16 v[16:31], v[154:157], v[204:207], v[16:31]
	v_max3_f32 v146, v146, v78, v79
	v_mov_b32_e32 v147, v146
	s_nop 1
	v_permlane32_swap_b32_e32 v146, v147
	v_max_f32_e32 v147, v147, v147
	v_max_f32_e32 v146, v146, v146
	v_max_f32_e32 v146, v146, v147
	v_sub_f32_e32 v147, v146, v201
	v_cmp_ge_f32_e32 vcc, s87, v147
	v_max_f32_e32 v147, v201, v201
	v_max_f32_e32 v147, v147, v146
	v_mfma_f32_32x32x16_bf16 v[16:31], v[158:161], v[208:211], v[16:31]
	v_sub_f32_e32 v146, v201, v147
	v_mul_f32_e32 v146, 0x3e0293ee, v146
	v_exp_f32_e32 v146, v146
	s_cmp_eq_u64 vcc, exec
	s_cselect_b64 s[42:43], -1, 0
	s_waitcnt vmcnt(0)
	s_barrier
	s_add_i32 m0, s52, 0x0
	s_nop 0
	global_load_lds_dwordx4 v232, s[48:49]
	s_add_i32 m0, s52, 0x400
	s_nop 0
	global_load_lds_dwordx4 v233, s[48:49]
	s_add_i32 m0, s53, 0x4000
	s_nop 0
	global_load_lds_dwordx4 v234, s[50:51]
	s_add_i32 m0, s53, 0x4400
	s_nop 0
	global_load_lds_dwordx4 v235, s[50:51]
	s_add_u32 s48, s48, 0x18000
	s_addc_u32 s49, s49, 0
	s_add_u32 s50, s50, 0xc0000
	s_addc_u32 s51, s51, 0
	v_cndmask_b32_e64 v146, v146, 1.0, s[42:43]
	v_cmp_gt_f32_e32 vcc, 1.0, v146
	s_cbranch_vccz .LBB0_464
	s_and_saveexec_b64 s[6:7], s[40:41]
	ds_write_b32 v184, v146 offset:128
	s_or_b64 exec, exec, s[6:7]
	s_waitcnt lgkmcnt(0)
	v_add_u32_e32 v142, v183, v96
	ds_read_b128 v[130:133], v142 offset:224
	ds_read_b128 v[134:137], v142 offset:192
	ds_read_b128 v[138:141], v142 offset:160
	ds_read_b128 v[142:145], v142 offset:128
	s_waitcnt lgkmcnt(3)
	v_pk_mul_f32 v[12:13], v[12:13], v[130:131]
	s_waitcnt lgkmcnt(2)
	v_pk_mul_f32 v[8:9], v[8:9], v[134:135]
	s_waitcnt lgkmcnt(1)
	v_pk_mul_f32 v[4:5], v[4:5], v[138:139]
	v_pk_mul_f32 v[14:15], v[14:15], v[132:133]
	v_pk_mul_f32 v[10:11], v[10:11], v[136:137]
	v_pk_mul_f32 v[6:7], v[6:7], v[140:141]
	s_waitcnt lgkmcnt(0)
	v_pk_mul_f32 v[2:3], v[2:3], v[144:145]
	v_pk_mul_f32 v[0:1], v[0:1], v[142:143]
	v_pk_mul_f32 v[60:61], v[60:61], v[130:131]
	v_pk_mul_f32 v[56:57], v[56:57], v[134:135]
	v_pk_mul_f32 v[52:53], v[52:53], v[138:139]
	v_pk_mul_f32 v[62:63], v[62:63], v[132:133]
	v_pk_mul_f32 v[58:59], v[58:59], v[136:137]
	v_pk_mul_f32 v[54:55], v[54:55], v[140:141]
	v_pk_mul_f32 v[50:51], v[50:51], v[144:145]
	v_pk_mul_f32 v[48:49], v[48:49], v[142:143]
	v_pk_mul_f32 v[44:45], v[44:45], v[130:131]
	v_pk_mul_f32 v[40:41], v[40:41], v[134:135]
	v_pk_mul_f32 v[36:37], v[36:37], v[138:139]
	v_pk_mul_f32 v[46:47], v[46:47], v[132:133]
	v_pk_mul_f32 v[42:43], v[42:43], v[136:137]
	v_pk_mul_f32 v[38:39], v[38:39], v[140:141]
	v_pk_mul_f32 v[34:35], v[34:35], v[144:145]
	v_pk_mul_f32 v[32:33], v[32:33], v[142:143]
	v_pk_mul_f32 v[28:29], v[28:29], v[130:131]
	v_pk_mul_f32 v[24:25], v[24:25], v[134:135]
	v_pk_mul_f32 v[20:21], v[20:21], v[138:139]
	v_pk_mul_f32 v[30:31], v[30:31], v[132:133]
	v_pk_mul_f32 v[26:27], v[26:27], v[136:137]
	v_pk_mul_f32 v[22:23], v[22:23], v[140:141]
	v_pk_mul_f32 v[18:19], v[18:19], v[144:145]
	v_pk_mul_f32 v[16:17], v[16:17], v[142:143]
; #define RESC(a) do { if (__any((a) < 1.f)) { if (hi == 0) al_l[r32] = (a); asm volatile("s_waitcnt lgkmcnt(0)" ::: "memory"); \
;     for (int d = 0; d < 4; ++d) for (int r = 0; r < 16; ++r) o[d][r] *= al_l[crow(r, hi)]; } } while (0)
; __device__ __forceinline__ void partialSM(f32x16& p0, f32x16& p1, float& m_reg, float& mn, float& alpha) {
;     ...
;   float mnC = -mn * C;
;   for (int r = 0; r < 16; ++r) p0[r] = fmaf(p0[r], C, mnC); for (int r = 0; r < 16; ++r) p1[r] = fmaf(p1[r], C, mnC);
;   for (int r = 0; r < 16; ++r) p0[r] = __builtin_amdgcn_exp2f(p0[r]);
; }
; __device__ __forceinline__ void finishSM(f32x16& p0, f32x16& p1, float alpha, float& l_reg, bf16x8& pa0, bf16x8& pa1, bf16x8& pa2, bf16x8& pa3) {
;   for (int r = 0; r < 16; ++r) p1[r] = __builtin_amdgcn_exp2f(p1[r]);
;   float ps = 0; for (int r = 0; r < 16; ++r) ps += p0[r]; for (int r = 0; r < 16; ++r) ps += p1[r];
;   { auto rr = __builtin_amdgcn_permlane32_swap(__float_as_uint(ps), __float_as_uint(ps), false, false);
;     ps = __uint_as_float(rr[0]) + __uint_as_float(rr[1]); }
;   l_reg = l_reg * alpha + ps;
; template <bool HALF> __device__ __forceinline__ void dense_body(const bf16_t* __restrict__ Qb, const bf16_t* __restrict__ Kh, const bf16_t* __restrict__ Vh, ...
;     ...
;     RESC(alA); __syncthreads();
;   }
.LBB0_464:
	v_cndmask_b32_e64 v150, v147, v201, s[42:43]
	v_mul_f32_e32 v130, 0xbe0293ee, v150
	v_mov_b32_e32 v131, v130
	v_fmamk_f32 v80, v80, 0x3e0293ee, v130
	v_fmamk_f32 v81, v81, 0x3e0293ee, v130
	v_fmamk_f32 v82, v82, 0x3e0293ee, v130
	v_fmamk_f32 v83, v83, 0x3e0293ee, v130
	v_fmamk_f32 v84, v84, 0x3e0293ee, v130
	v_fmamk_f32 v85, v85, 0x3e0293ee, v130
	v_fmamk_f32 v86, v86, 0x3e0293ee, v130
	v_fmamk_f32 v87, v87, 0x3e0293ee, v130
	v_fmamk_f32 v88, v88, 0x3e0293ee, v130
	v_fmamk_f32 v89, v89, 0x3e0293ee, v130
	v_fmamk_f32 v90, v90, 0x3e0293ee, v130
	v_fmamk_f32 v91, v91, 0x3e0293ee, v130
	v_fmamk_f32 v92, v92, 0x3e0293ee, v130
	v_fmamk_f32 v93, v93, 0x3e0293ee, v130
	v_fmamk_f32 v94, v94, 0x3e0293ee, v130
	v_fmac_f32_e32 v131, 0x3e0293ee, v95
	v_exp_f32_e32 v147, v80
	v_exp_f32_e32 v160, v81
	v_exp_f32_e32 v148, v82
	v_exp_f32_e32 v161, v83
	v_exp_f32_e32 v149, v84
	v_exp_f32_e32 v170, v85
	v_exp_f32_e32 v159, v86
	v_exp_f32_e32 v171, v87
	v_exp_f32_e32 v151, v88
	v_exp_f32_e32 v155, v89
	v_exp_f32_e32 v152, v90
	v_exp_f32_e32 v156, v91
	v_exp_f32_e32 v153, v92
	v_exp_f32_e32 v157, v93
	v_exp_f32_e32 v154, v94
	v_exp_f32_e32 v158, v131
	v_pk_fma_f32 v[144:145], v[64:65], s[10:11], v[130:131] op_sel_hi:[1,0,0]
	v_add_f32_e32 v64, v198, v199
	v_fmac_f32_e32 v64, v197, v185
	v_add_f32_e32 v185, v202, v203
	v_pk_fma_f32 v[142:143], v[66:67], s[10:11], v[130:131] op_sel_hi:[1,0,0]
	v_pk_fma_f32 v[138:139], v[68:69], s[10:11], v[130:131] op_sel_hi:[1,0,0]
	v_pk_fma_f32 v[134:135], v[70:71], s[10:11], v[130:131] op_sel_hi:[1,0,0]
	v_pk_fma_f32 v[132:133], v[72:73], s[10:11], v[130:131] op_sel_hi:[1,0,0]
	v_pk_fma_f32 v[140:141], v[74:75], s[10:11], v[130:131] op_sel_hi:[1,0,0]
	v_pk_fma_f32 v[136:137], v[76:77], s[10:11], v[130:131] op_sel_hi:[1,0,0]
	v_pk_fma_f32 v[130:131], v[78:79], s[10:11], v[130:131] op_sel_hi:[1,0,0]
	v_fmac_f32_e32 v185, v64, v200
	s_add_i32 s3, s3, 2
	s_and_b64 vcc, exec, s[14:15]
	s_waitcnt lgkmcnt(0)
	s_cbranch_vccnz .LBB0_466
	v_mov_b32_e32 v197, v146
	s_branch .LBB0_454
